# hand-written expert-weight converter (fp8 before LDS transpose, 3 items in flight, nt loads), CONV_WGS 80
# speedup vs baseline: 1.0055x; 1.0055x over previous
.LBB0_280:
	v_readlane_b32 s2, v253, 6
	v_readlane_b32 s3, v253, 7
	s_cmp_lt_i32 s2, 3
	s_cselect_b64 s[2:3], -1, 0
	s_and_b64 s[0:1], s[2:3], s[0:1]
	s_andn2_b64 vcc, exec, s[0:1]
	s_cbranch_vccnz .LBB0_477
	s_cmpk_eq_i32 s84, 0x100
	s_cselect_b32 s12, 0x50, 0
	v_mbcnt_lo_u32_b32 v0, -1, 0
	s_sub_i32 s29, s84, s12
	v_mbcnt_hi_u32_b32 v144, -1, v0
	s_cmp_lt_i32 s87, s29
	s_mov_b64 s[2:3], -1
	s_cbranch_scc1 .LBB0_312
	s_sub_i32 s8, s87, s29
	s_lshl_b32 s2, s8, 3
	s_add_i32 s2, s2, s86
	s_cmp_gt_u32 s2, 0x17fff
	s_cbranch_scc1 .LBB0_311
	s_lshl_b32 s3, s12, 3
	s_mul_i32 s31, s3, 3
	s_waitcnt vmcnt(0)
	v_mbcnt_lo_u32_b32 v240, -1, 0
	v_mbcnt_hi_u32_b32 v240, -1, v240
	v_lshrrev_b32_e32 v241, 3, v240
	v_and_b32_e32 v242, 7, v240
	v_lshlrev_b32_e32 v243, 4, v242
	v_lshl_add_u32 v244, v241, 14, v243
	v_lshl_add_u32 v245, v241, 13, v243
	v_lshl_add_u32 v249, v241, 13, v243
	s_mul_i32 s22, s86, 0x4200
	s_movk_i32 s23, 0x210
	v_mul_u32_u24_e32 v247, s23, v242
	v_lshl_add_u32 v247, v241, 2, v247
	v_add_u32_e32 v247, s22, v247
	v_mul_u32_u24_e32 v248, s23, v241
	v_lshl_add_u32 v248, v242, 6, v248
	v_add_u32_e32 v248, s22, v248
	v_mov_b32_e32 v250, 0x43e00000
	s_mov_b32 s15, 0xc3e00000
	s_mov_b32 s16, 0x5010400
	s_mov_b32 s17, 0x7030602
	s_mov_b32 s18, 0x5040100
	s_mov_b32 s19, 0x7060302
	s_mov_b32 s28, 0x17fff
	s_min_u32 s22, s2, s28
	s_cmp_lt_u32 s22, 0x10000
	s_cbranch_scc0 .Lcv_dn_0
	s_lshr_b32 s23, s22, 11
	s_bfe_u32 s24, s22, 0x40007
	s_and_b32 s25, s22, 0x7f
	s_lshl_b32 s30, s24, 7
	s_lshl_b32 s24, s24, 21
	s_lshl_b32 s22, s25, 7
	s_add_u32 s24, s24, s22
	s_lshl_b32 s25, s25, 16
	s_add_u32 s30, s30, s25
	s_lshl_b32 s22, s23, 25
	s_add_u32 s24, s24, s22
	s_add_u32 s4, s70, s24
	s_addc_u32 s5, s71, 0
	s_lshl_b32 s23, s23, 23
	s_add_u32 s30, s30, s23
	s_add_u32 s30, s30, 0x38ee1c00
	s_add_u32 s6, s92, s30
	s_addc_u32 s7, s93, 0
	s_mov_b32 s14, 0x20000
	s_mov_b64 vcc, -1
	s_branch .Lcv_ld_0
.Lcv_dn_0:
	s_sub_u32 s22, s22, 0x10000
	s_lshr_b32 s23, s22, 10
	s_bfe_u32 s24, s22, 0x40006
	s_and_b32 s25, s22, 0x3f
	s_lshl_b32 s30, s24, 7
	s_lshl_b32 s24, s24, 20
	s_lshl_b32 s22, s25, 7
	s_add_u32 s24, s24, s22
	s_lshl_b32 s25, s25, 16
	s_add_u32 s30, s30, s25
	s_lshl_b32 s22, s23, 24
	s_add_u32 s24, s24, s22
	s_add_u32 s4, s74, s24
	s_addc_u32 s5, s75, 0
	s_lshl_b32 s23, s23, 22
	s_add_u32 s30, s30, s23
	s_add_u32 s30, s30, 0x48ee1c00
	s_add_u32 s6, s92, s30
	s_addc_u32 s7, s93, 0
	s_mov_b32 s14, 0x10000
	s_mov_b64 vcc, 0
.Lcv_ld_0:
	s_add_u32 s2, s2, s3
	v_cndmask_b32_e32 v246, v245, v244, vcc
	global_load_dwordx4 v[0:3], v246, s[4:5] nt
	s_add_u32 s4, s4, s14
	s_addc_u32 s5, s5, 0
	global_load_dwordx4 v[4:7], v246, s[4:5] nt
	s_add_u32 s4, s4, s14
	s_addc_u32 s5, s5, 0
	global_load_dwordx4 v[8:11], v246, s[4:5] nt
	s_add_u32 s4, s4, s14
	s_addc_u32 s5, s5, 0
	global_load_dwordx4 v[12:15], v246, s[4:5] nt
	s_add_u32 s4, s4, s14
	s_addc_u32 s5, s5, 0
	global_load_dwordx4 v[16:19], v246, s[4:5] nt
	s_add_u32 s4, s4, s14
	s_addc_u32 s5, s5, 0
	global_load_dwordx4 v[20:23], v246, s[4:5] nt
	s_add_u32 s4, s4, s14
	s_addc_u32 s5, s5, 0
	global_load_dwordx4 v[24:27], v246, s[4:5] nt
	s_add_u32 s4, s4, s14
	s_addc_u32 s5, s5, 0
	global_load_dwordx4 v[28:31], v246, s[4:5] nt
	s_add_u32 s4, s4, s14
	s_addc_u32 s5, s5, 0
	global_load_dwordx4 v[32:35], v246, s[4:5] nt
	s_add_u32 s4, s4, s14
	s_addc_u32 s5, s5, 0
	global_load_dwordx4 v[36:39], v246, s[4:5] nt
	s_add_u32 s4, s4, s14
	s_addc_u32 s5, s5, 0
	global_load_dwordx4 v[40:43], v246, s[4:5] nt
	s_add_u32 s4, s4, s14
	s_addc_u32 s5, s5, 0
	global_load_dwordx4 v[44:47], v246, s[4:5] nt
	s_add_u32 s4, s4, s14
	s_addc_u32 s5, s5, 0
	global_load_dwordx4 v[48:51], v246, s[4:5] nt
	s_add_u32 s4, s4, s14
	s_addc_u32 s5, s5, 0
	global_load_dwordx4 v[52:55], v246, s[4:5] nt
	s_add_u32 s4, s4, s14
	s_addc_u32 s5, s5, 0
	global_load_dwordx4 v[56:59], v246, s[4:5] nt
	s_add_u32 s4, s4, s14
	s_addc_u32 s5, s5, 0
	global_load_dwordx4 v[60:63], v246, s[4:5] nt
	s_min_u32 s22, s2, s28
	s_cmp_lt_u32 s22, 0x10000
	s_cbranch_scc0 .Lcv_dn_1
	s_lshr_b32 s23, s22, 11
	s_bfe_u32 s24, s22, 0x40007
	s_and_b32 s25, s22, 0x7f
	s_lshl_b32 s30, s24, 7
	s_lshl_b32 s24, s24, 21
	s_lshl_b32 s22, s25, 7
	s_add_u32 s24, s24, s22
	s_lshl_b32 s25, s25, 16
	s_add_u32 s30, s30, s25
	s_lshl_b32 s22, s23, 25
	s_add_u32 s24, s24, s22
	s_add_u32 s4, s70, s24
	s_addc_u32 s5, s71, 0
	s_lshl_b32 s23, s23, 23
	s_add_u32 s30, s30, s23
	s_add_u32 s30, s30, 0x38ee1c00
	s_add_u32 s8, s92, s30
	s_addc_u32 s9, s93, 0
	s_mov_b32 s14, 0x20000
	s_mov_b64 vcc, -1
	s_branch .Lcv_ld_1
.Lcv_dn_1:
	s_sub_u32 s22, s22, 0x10000
	s_lshr_b32 s23, s22, 10
	s_bfe_u32 s24, s22, 0x40006
	s_and_b32 s25, s22, 0x3f
	s_lshl_b32 s30, s24, 7
	s_lshl_b32 s24, s24, 20
	s_lshl_b32 s22, s25, 7
	s_add_u32 s24, s24, s22
	s_lshl_b32 s25, s25, 16
	s_add_u32 s30, s30, s25
	s_lshl_b32 s22, s23, 24
	s_add_u32 s24, s24, s22
	s_add_u32 s4, s74, s24
	s_addc_u32 s5, s75, 0
	s_lshl_b32 s23, s23, 22
	s_add_u32 s30, s30, s23
	s_add_u32 s30, s30, 0x48ee1c00
	s_add_u32 s8, s92, s30
	s_addc_u32 s9, s93, 0
	s_mov_b32 s14, 0x10000
	s_mov_b64 vcc, 0
.Lcv_ld_1:
	s_add_u32 s2, s2, s3
	v_cndmask_b32_e32 v246, v245, v244, vcc
	global_load_dwordx4 v[64:67], v246, s[4:5] nt
	s_add_u32 s4, s4, s14
	s_addc_u32 s5, s5, 0
	global_load_dwordx4 v[68:71], v246, s[4:5] nt
	s_add_u32 s4, s4, s14
	s_addc_u32 s5, s5, 0
	global_load_dwordx4 v[72:75], v246, s[4:5] nt
	s_add_u32 s4, s4, s14
	s_addc_u32 s5, s5, 0
	global_load_dwordx4 v[76:79], v246, s[4:5] nt
	s_add_u32 s4, s4, s14
	s_addc_u32 s5, s5, 0
	global_load_dwordx4 v[80:83], v246, s[4:5] nt
	s_add_u32 s4, s4, s14
	s_addc_u32 s5, s5, 0
	global_load_dwordx4 v[84:87], v246, s[4:5] nt
	s_add_u32 s4, s4, s14
	s_addc_u32 s5, s5, 0
	global_load_dwordx4 v[88:91], v246, s[4:5] nt
	s_add_u32 s4, s4, s14
	s_addc_u32 s5, s5, 0
	global_load_dwordx4 v[92:95], v246, s[4:5] nt
	s_add_u32 s4, s4, s14
	s_addc_u32 s5, s5, 0
	global_load_dwordx4 v[96:99], v246, s[4:5] nt
	s_add_u32 s4, s4, s14
	s_addc_u32 s5, s5, 0
	global_load_dwordx4 v[100:103], v246, s[4:5] nt
	s_add_u32 s4, s4, s14
	s_addc_u32 s5, s5, 0
	global_load_dwordx4 v[104:107], v246, s[4:5] nt
	s_add_u32 s4, s4, s14
	s_addc_u32 s5, s5, 0
	global_load_dwordx4 v[108:111], v246, s[4:5] nt
	s_add_u32 s4, s4, s14
	s_addc_u32 s5, s5, 0
	global_load_dwordx4 v[112:115], v246, s[4:5] nt
	s_add_u32 s4, s4, s14
	s_addc_u32 s5, s5, 0
	global_load_dwordx4 v[116:119], v246, s[4:5] nt
	s_add_u32 s4, s4, s14
	s_addc_u32 s5, s5, 0
	global_load_dwordx4 v[120:123], v246, s[4:5] nt
	s_add_u32 s4, s4, s14
	s_addc_u32 s5, s5, 0
	global_load_dwordx4 v[124:127], v246, s[4:5] nt
	s_min_u32 s22, s2, s28
	s_cmp_lt_u32 s22, 0x10000
	s_cbranch_scc0 .Lcv_dn_2
	s_lshr_b32 s23, s22, 11
	s_bfe_u32 s24, s22, 0x40007
	s_and_b32 s25, s22, 0x7f
	s_lshl_b32 s30, s24, 7
	s_lshl_b32 s24, s24, 21
	s_lshl_b32 s22, s25, 7
	s_add_u32 s24, s24, s22
	s_lshl_b32 s25, s25, 16
	s_add_u32 s30, s30, s25
	s_lshl_b32 s22, s23, 25
	s_add_u32 s24, s24, s22
	s_add_u32 s4, s70, s24
	s_addc_u32 s5, s71, 0
	s_lshl_b32 s23, s23, 23
	s_add_u32 s30, s30, s23
	s_add_u32 s30, s30, 0x38ee1c00
	s_add_u32 s10, s92, s30
	s_addc_u32 s11, s93, 0
	s_mov_b32 s14, 0x20000
	s_mov_b64 vcc, -1
	s_branch .Lcv_ld_2
.Lcv_dn_2:
	s_sub_u32 s22, s22, 0x10000
	s_lshr_b32 s23, s22, 10
	s_bfe_u32 s24, s22, 0x40006
	s_and_b32 s25, s22, 0x3f
	s_lshl_b32 s30, s24, 7
	s_lshl_b32 s24, s24, 20
	s_lshl_b32 s22, s25, 7
	s_add_u32 s24, s24, s22
	s_lshl_b32 s25, s25, 16
	s_add_u32 s30, s30, s25
	s_lshl_b32 s22, s23, 24
	s_add_u32 s24, s24, s22
	s_add_u32 s4, s74, s24
	s_addc_u32 s5, s75, 0
	s_lshl_b32 s23, s23, 22
	s_add_u32 s30, s30, s23
	s_add_u32 s30, s30, 0x48ee1c00
	s_add_u32 s10, s92, s30
	s_addc_u32 s11, s93, 0
	s_mov_b32 s14, 0x10000
	s_mov_b64 vcc, 0
.Lcv_ld_2:
	s_add_u32 s2, s2, s3
	v_cndmask_b32_e32 v246, v245, v244, vcc
	global_load_dwordx4 v[128:131], v246, s[4:5] nt
	s_add_u32 s4, s4, s14
	s_addc_u32 s5, s5, 0
	global_load_dwordx4 v[132:135], v246, s[4:5] nt
	s_add_u32 s4, s4, s14
	s_addc_u32 s5, s5, 0
	global_load_dwordx4 v[136:139], v246, s[4:5] nt
	s_add_u32 s4, s4, s14
	s_addc_u32 s5, s5, 0
	global_load_dwordx4 v[140:143], v246, s[4:5] nt
	s_add_u32 s4, s4, s14
	s_addc_u32 s5, s5, 0
	global_load_dwordx4 v[144:147], v246, s[4:5] nt
	s_add_u32 s4, s4, s14
	s_addc_u32 s5, s5, 0
	global_load_dwordx4 v[148:151], v246, s[4:5] nt
	s_add_u32 s4, s4, s14
	s_addc_u32 s5, s5, 0
	global_load_dwordx4 v[152:155], v246, s[4:5] nt
	s_add_u32 s4, s4, s14
	s_addc_u32 s5, s5, 0
	global_load_dwordx4 v[156:159], v246, s[4:5] nt
	s_add_u32 s4, s4, s14
	s_addc_u32 s5, s5, 0
	global_load_dwordx4 v[160:163], v246, s[4:5] nt
	s_add_u32 s4, s4, s14
	s_addc_u32 s5, s5, 0
	global_load_dwordx4 v[164:167], v246, s[4:5] nt
	s_add_u32 s4, s4, s14
	s_addc_u32 s5, s5, 0
	global_load_dwordx4 v[168:171], v246, s[4:5] nt
	s_add_u32 s4, s4, s14
	s_addc_u32 s5, s5, 0
	global_load_dwordx4 v[172:175], v246, s[4:5] nt
	s_add_u32 s4, s4, s14
	s_addc_u32 s5, s5, 0
	global_load_dwordx4 v[176:179], v246, s[4:5] nt
	s_add_u32 s4, s4, s14
	s_addc_u32 s5, s5, 0
	global_load_dwordx4 v[180:183], v246, s[4:5] nt
	s_add_u32 s4, s4, s14
	s_addc_u32 s5, s5, 0
	global_load_dwordx4 v[184:187], v246, s[4:5] nt
	s_add_u32 s4, s4, s14
	s_addc_u32 s5, s5, 0
	global_load_dwordx4 v[188:191], v246, s[4:5] nt
	s_waitcnt vmcnt(32)
	v_mul_f32_e32 v0, 0x42800000, v0
	v_mul_f32_e32 v1, 0x42800000, v1
	v_mul_f32_e32 v2, 0x42800000, v2
	v_mul_f32_e32 v3, 0x42800000, v3
	v_med3_f32 v0, v0, s15, v250
	v_med3_f32 v1, v1, s15, v250
	v_med3_f32 v2, v2, s15, v250
	v_med3_f32 v3, v3, s15, v250
	v_cvt_pk_fp8_f32 v192, v0, v1
	v_cvt_pk_fp8_f32 v192, v2, v3 op_sel:[0,0,1]
	v_mul_f32_e32 v4, 0x42800000, v4
	v_mul_f32_e32 v5, 0x42800000, v5
	v_mul_f32_e32 v6, 0x42800000, v6
	v_mul_f32_e32 v7, 0x42800000, v7
	v_med3_f32 v4, v4, s15, v250
	v_med3_f32 v5, v5, s15, v250
	v_med3_f32 v6, v6, s15, v250
	v_med3_f32 v7, v7, s15, v250
	v_cvt_pk_fp8_f32 v193, v4, v5
	v_cvt_pk_fp8_f32 v193, v6, v7 op_sel:[0,0,1]
	v_mul_f32_e32 v8, 0x42800000, v8
	v_mul_f32_e32 v9, 0x42800000, v9
	v_mul_f32_e32 v10, 0x42800000, v10
	v_mul_f32_e32 v11, 0x42800000, v11
	v_med3_f32 v8, v8, s15, v250
	v_med3_f32 v9, v9, s15, v250
	v_med3_f32 v10, v10, s15, v250
	v_med3_f32 v11, v11, s15, v250
	v_cvt_pk_fp8_f32 v194, v8, v9
	v_cvt_pk_fp8_f32 v194, v10, v11 op_sel:[0,0,1]
	v_mul_f32_e32 v12, 0x42800000, v12
	v_mul_f32_e32 v13, 0x42800000, v13
	v_mul_f32_e32 v14, 0x42800000, v14
	v_mul_f32_e32 v15, 0x42800000, v15
	v_med3_f32 v12, v12, s15, v250
	v_med3_f32 v13, v13, s15, v250
	v_med3_f32 v14, v14, s15, v250
	v_med3_f32 v15, v15, s15, v250
	v_cvt_pk_fp8_f32 v195, v12, v13
	v_cvt_pk_fp8_f32 v195, v14, v15 op_sel:[0,0,1]
	v_mul_f32_e32 v16, 0x42800000, v16
	v_mul_f32_e32 v17, 0x42800000, v17
	v_mul_f32_e32 v18, 0x42800000, v18
	v_mul_f32_e32 v19, 0x42800000, v19
	v_med3_f32 v16, v16, s15, v250
	v_med3_f32 v17, v17, s15, v250
	v_med3_f32 v18, v18, s15, v250
	v_med3_f32 v19, v19, s15, v250
	v_cvt_pk_fp8_f32 v196, v16, v17
	v_cvt_pk_fp8_f32 v196, v18, v19 op_sel:[0,0,1]
	v_mul_f32_e32 v20, 0x42800000, v20
	v_mul_f32_e32 v21, 0x42800000, v21
	v_mul_f32_e32 v22, 0x42800000, v22
	v_mul_f32_e32 v23, 0x42800000, v23
	v_med3_f32 v20, v20, s15, v250
	v_med3_f32 v21, v21, s15, v250
	v_med3_f32 v22, v22, s15, v250
	v_med3_f32 v23, v23, s15, v250
	v_cvt_pk_fp8_f32 v197, v20, v21
	v_cvt_pk_fp8_f32 v197, v22, v23 op_sel:[0,0,1]
	v_mul_f32_e32 v24, 0x42800000, v24
	v_mul_f32_e32 v25, 0x42800000, v25
	v_mul_f32_e32 v26, 0x42800000, v26
	v_mul_f32_e32 v27, 0x42800000, v27
	v_med3_f32 v24, v24, s15, v250
	v_med3_f32 v25, v25, s15, v250
	v_med3_f32 v26, v26, s15, v250
	v_med3_f32 v27, v27, s15, v250
	v_cvt_pk_fp8_f32 v198, v24, v25
	v_cvt_pk_fp8_f32 v198, v26, v27 op_sel:[0,0,1]
	v_mul_f32_e32 v28, 0x42800000, v28
	v_mul_f32_e32 v29, 0x42800000, v29
	v_mul_f32_e32 v30, 0x42800000, v30
	v_mul_f32_e32 v31, 0x42800000, v31
	v_med3_f32 v28, v28, s15, v250
	v_med3_f32 v29, v29, s15, v250
	v_med3_f32 v30, v30, s15, v250
	v_med3_f32 v31, v31, s15, v250
	v_cvt_pk_fp8_f32 v199, v28, v29
	v_cvt_pk_fp8_f32 v199, v30, v31 op_sel:[0,0,1]
	v_mul_f32_e32 v32, 0x42800000, v32
	v_mul_f32_e32 v33, 0x42800000, v33
	v_mul_f32_e32 v34, 0x42800000, v34
	v_mul_f32_e32 v35, 0x42800000, v35
	v_med3_f32 v32, v32, s15, v250
	v_med3_f32 v33, v33, s15, v250
	v_med3_f32 v34, v34, s15, v250
	v_med3_f32 v35, v35, s15, v250
	v_cvt_pk_fp8_f32 v200, v32, v33
	v_cvt_pk_fp8_f32 v200, v34, v35 op_sel:[0,0,1]
	v_mul_f32_e32 v36, 0x42800000, v36
	v_mul_f32_e32 v37, 0x42800000, v37
	v_mul_f32_e32 v38, 0x42800000, v38
	v_mul_f32_e32 v39, 0x42800000, v39
	v_med3_f32 v36, v36, s15, v250
	v_med3_f32 v37, v37, s15, v250
	v_med3_f32 v38, v38, s15, v250
	v_med3_f32 v39, v39, s15, v250
	v_cvt_pk_fp8_f32 v201, v36, v37
	v_cvt_pk_fp8_f32 v201, v38, v39 op_sel:[0,0,1]
	v_mul_f32_e32 v40, 0x42800000, v40
	v_mul_f32_e32 v41, 0x42800000, v41
	v_mul_f32_e32 v42, 0x42800000, v42
	v_mul_f32_e32 v43, 0x42800000, v43
	v_med3_f32 v40, v40, s15, v250
	v_med3_f32 v41, v41, s15, v250
	v_med3_f32 v42, v42, s15, v250
	v_med3_f32 v43, v43, s15, v250
	v_cvt_pk_fp8_f32 v202, v40, v41
	v_cvt_pk_fp8_f32 v202, v42, v43 op_sel:[0,0,1]
	v_mul_f32_e32 v44, 0x42800000, v44
	v_mul_f32_e32 v45, 0x42800000, v45
	v_mul_f32_e32 v46, 0x42800000, v46
	v_mul_f32_e32 v47, 0x42800000, v47
	v_med3_f32 v44, v44, s15, v250
	v_med3_f32 v45, v45, s15, v250
	v_med3_f32 v46, v46, s15, v250
	v_med3_f32 v47, v47, s15, v250
	v_cvt_pk_fp8_f32 v203, v44, v45
	v_cvt_pk_fp8_f32 v203, v46, v47 op_sel:[0,0,1]
	v_mul_f32_e32 v48, 0x42800000, v48
	v_mul_f32_e32 v49, 0x42800000, v49
	v_mul_f32_e32 v50, 0x42800000, v50
	v_mul_f32_e32 v51, 0x42800000, v51
	v_med3_f32 v48, v48, s15, v250
	v_med3_f32 v49, v49, s15, v250
	v_med3_f32 v50, v50, s15, v250
	v_med3_f32 v51, v51, s15, v250
	v_cvt_pk_fp8_f32 v204, v48, v49
	v_cvt_pk_fp8_f32 v204, v50, v51 op_sel:[0,0,1]
	v_mul_f32_e32 v52, 0x42800000, v52
	v_mul_f32_e32 v53, 0x42800000, v53
	v_mul_f32_e32 v54, 0x42800000, v54
	v_mul_f32_e32 v55, 0x42800000, v55
	v_med3_f32 v52, v52, s15, v250
	v_med3_f32 v53, v53, s15, v250
	v_med3_f32 v54, v54, s15, v250
	v_med3_f32 v55, v55, s15, v250
	v_cvt_pk_fp8_f32 v205, v52, v53
	v_cvt_pk_fp8_f32 v205, v54, v55 op_sel:[0,0,1]
	v_mul_f32_e32 v56, 0x42800000, v56
	v_mul_f32_e32 v57, 0x42800000, v57
	v_mul_f32_e32 v58, 0x42800000, v58
	v_mul_f32_e32 v59, 0x42800000, v59
	v_med3_f32 v56, v56, s15, v250
	v_med3_f32 v57, v57, s15, v250
	v_med3_f32 v58, v58, s15, v250
	v_med3_f32 v59, v59, s15, v250
	v_cvt_pk_fp8_f32 v206, v56, v57
	v_cvt_pk_fp8_f32 v206, v58, v59 op_sel:[0,0,1]
	v_mul_f32_e32 v60, 0x42800000, v60
	v_mul_f32_e32 v61, 0x42800000, v61
	v_mul_f32_e32 v62, 0x42800000, v62
	v_mul_f32_e32 v63, 0x42800000, v63
	v_med3_f32 v60, v60, s15, v250
	v_med3_f32 v61, v61, s15, v250
	v_med3_f32 v62, v62, s15, v250
	v_med3_f32 v63, v63, s15, v250
	v_cvt_pk_fp8_f32 v207, v60, v61
	v_cvt_pk_fp8_f32 v207, v62, v63 op_sel:[0,0,1]
	s_min_u32 s22, s2, s28
	s_cmp_lt_u32 s22, 0x10000
	s_cbranch_scc0 .Lcv_dn_3
	s_lshr_b32 s23, s22, 11
	s_bfe_u32 s24, s22, 0x40007
	s_and_b32 s25, s22, 0x7f
	s_lshl_b32 s30, s24, 7
	s_lshl_b32 s24, s24, 21
	s_lshl_b32 s22, s25, 7
	s_add_u32 s24, s24, s22
	s_lshl_b32 s25, s25, 16
	s_add_u32 s30, s30, s25
	s_lshl_b32 s22, s23, 25
	s_add_u32 s24, s24, s22
	s_add_u32 s4, s70, s24
	s_addc_u32 s5, s71, 0
	s_lshl_b32 s23, s23, 23
	s_add_u32 s30, s30, s23
	s_add_u32 s30, s30, 0x38ee1c00
	s_add_u32 s20, s92, s30
	s_addc_u32 s21, s93, 0
	s_mov_b32 s14, 0x20000
	s_mov_b64 vcc, -1
	s_branch .Lcv_ld_3
.Lcv_dn_3:
	s_sub_u32 s22, s22, 0x10000
	s_lshr_b32 s23, s22, 10
	s_bfe_u32 s24, s22, 0x40006
	s_and_b32 s25, s22, 0x3f
	s_lshl_b32 s30, s24, 7
	s_lshl_b32 s24, s24, 20
	s_lshl_b32 s22, s25, 7
	s_add_u32 s24, s24, s22
	s_lshl_b32 s25, s25, 16
	s_add_u32 s30, s30, s25
	s_lshl_b32 s22, s23, 24
	s_add_u32 s24, s24, s22
	s_add_u32 s4, s74, s24
	s_addc_u32 s5, s75, 0
	s_lshl_b32 s23, s23, 22
	s_add_u32 s30, s30, s23
	s_add_u32 s30, s30, 0x48ee1c00
	s_add_u32 s20, s92, s30
	s_addc_u32 s21, s93, 0
	s_mov_b32 s14, 0x10000
	s_mov_b64 vcc, 0
.Lcv_ld_3:
	s_add_u32 s2, s2, s3
	v_cndmask_b32_e32 v246, v245, v244, vcc
	global_load_dwordx4 v[0:3], v246, s[4:5] nt
	s_add_u32 s4, s4, s14
	s_addc_u32 s5, s5, 0
	global_load_dwordx4 v[4:7], v246, s[4:5] nt
	s_add_u32 s4, s4, s14
	s_addc_u32 s5, s5, 0
	global_load_dwordx4 v[8:11], v246, s[4:5] nt
	s_add_u32 s4, s4, s14
	s_addc_u32 s5, s5, 0
	global_load_dwordx4 v[12:15], v246, s[4:5] nt
	s_add_u32 s4, s4, s14
	s_addc_u32 s5, s5, 0
	global_load_dwordx4 v[16:19], v246, s[4:5] nt
	s_add_u32 s4, s4, s14
	s_addc_u32 s5, s5, 0
	global_load_dwordx4 v[20:23], v246, s[4:5] nt
	s_add_u32 s4, s4, s14
	s_addc_u32 s5, s5, 0
	global_load_dwordx4 v[24:27], v246, s[4:5] nt
	s_add_u32 s4, s4, s14
	s_addc_u32 s5, s5, 0
	global_load_dwordx4 v[28:31], v246, s[4:5] nt
	s_add_u32 s4, s4, s14
	s_addc_u32 s5, s5, 0
	global_load_dwordx4 v[32:35], v246, s[4:5] nt
	s_add_u32 s4, s4, s14
	s_addc_u32 s5, s5, 0
	global_load_dwordx4 v[36:39], v246, s[4:5] nt
	s_add_u32 s4, s4, s14
	s_addc_u32 s5, s5, 0
	global_load_dwordx4 v[40:43], v246, s[4:5] nt
	s_add_u32 s4, s4, s14
	s_addc_u32 s5, s5, 0
	global_load_dwordx4 v[44:47], v246, s[4:5] nt
	s_add_u32 s4, s4, s14
	s_addc_u32 s5, s5, 0
	global_load_dwordx4 v[48:51], v246, s[4:5] nt
	s_add_u32 s4, s4, s14
	s_addc_u32 s5, s5, 0
	global_load_dwordx4 v[52:55], v246, s[4:5] nt
	s_add_u32 s4, s4, s14
	s_addc_u32 s5, s5, 0
	global_load_dwordx4 v[56:59], v246, s[4:5] nt
	s_add_u32 s4, s4, s14
	s_addc_u32 s5, s5, 0
	global_load_dwordx4 v[60:63], v246, s[4:5] nt
	ds_write_b32 v247, v192 offset:0
	ds_write_b32 v247, v193 offset:32
	ds_write_b32 v247, v194 offset:64
	ds_write_b32 v247, v195 offset:96
	ds_write_b32 v247, v196 offset:128
	ds_write_b32 v247, v197 offset:160
	ds_write_b32 v247, v198 offset:192
	ds_write_b32 v247, v199 offset:224
	ds_write_b32 v247, v200 offset:256
	ds_write_b32 v247, v201 offset:288
	ds_write_b32 v247, v202 offset:320
	ds_write_b32 v247, v203 offset:352
	ds_write_b32 v247, v204 offset:384
	ds_write_b32 v247, v205 offset:416
	ds_write_b32 v247, v206 offset:448
	ds_write_b32 v247, v207 offset:480
	ds_read_b128 v[208:211], v248 offset:0
	ds_read_b128 v[212:215], v248 offset:16
	ds_read_b128 v[216:219], v248 offset:32
	ds_read_b128 v[220:223], v248 offset:48
	s_waitcnt lgkmcnt(3)
	v_perm_b32 v240, v209, v208, s16
	v_perm_b32 v241, v209, v208, s17
	v_perm_b32 v242, v211, v210, s16
	v_perm_b32 v243, v211, v210, s17
	v_perm_b32 v224, v242, v240, s18
	v_perm_b32 v228, v242, v240, s19
	v_perm_b32 v232, v243, v241, s18
	v_perm_b32 v236, v243, v241, s19
	s_waitcnt lgkmcnt(2)
	v_perm_b32 v240, v213, v212, s16
	v_perm_b32 v241, v213, v212, s17
	v_perm_b32 v242, v215, v214, s16
	v_perm_b32 v243, v215, v214, s17
	v_perm_b32 v225, v242, v240, s18
	v_perm_b32 v229, v242, v240, s19
	v_perm_b32 v233, v243, v241, s18
	v_perm_b32 v237, v243, v241, s19
	s_waitcnt lgkmcnt(1)
	v_perm_b32 v240, v217, v216, s16
	v_perm_b32 v241, v217, v216, s17
	v_perm_b32 v242, v219, v218, s16
	v_perm_b32 v243, v219, v218, s17
	v_perm_b32 v226, v242, v240, s18
	v_perm_b32 v230, v242, v240, s19
	v_perm_b32 v234, v243, v241, s18
	v_perm_b32 v238, v243, v241, s19
	s_waitcnt lgkmcnt(0)
	v_perm_b32 v240, v221, v220, s16
	v_perm_b32 v241, v221, v220, s17
	v_perm_b32 v242, v223, v222, s16
	v_perm_b32 v243, v223, v222, s17
	v_perm_b32 v227, v242, v240, s18
	v_perm_b32 v231, v242, v240, s19
	v_perm_b32 v235, v243, v241, s18
	v_perm_b32 v239, v243, v241, s19
	s_add_u32 s26, s6, 0x1000
	s_addc_u32 s27, s7, 0
	global_store_dwordx4 v249, v[224:227], s[6:7]
	global_store_dwordx4 v249, v[228:231], s[6:7] offset:2048
	global_store_dwordx4 v249, v[232:235], s[26:27]
	global_store_dwordx4 v249, v[236:239], s[26:27] offset:2048
	s_mov_b64 s[6:7], s[20:21]
	s_waitcnt vmcnt(36)
	v_mul_f32_e32 v64, 0x42800000, v64
	v_mul_f32_e32 v65, 0x42800000, v65
	v_mul_f32_e32 v66, 0x42800000, v66
	v_mul_f32_e32 v67, 0x42800000, v67
	v_med3_f32 v64, v64, s15, v250
	v_med3_f32 v65, v65, s15, v250
	v_med3_f32 v66, v66, s15, v250
	v_med3_f32 v67, v67, s15, v250
	v_cvt_pk_fp8_f32 v192, v64, v65
	v_cvt_pk_fp8_f32 v192, v66, v67 op_sel:[0,0,1]
	v_mul_f32_e32 v68, 0x42800000, v68
	v_mul_f32_e32 v69, 0x42800000, v69
	v_mul_f32_e32 v70, 0x42800000, v70
	v_mul_f32_e32 v71, 0x42800000, v71
	v_med3_f32 v68, v68, s15, v250
	v_med3_f32 v69, v69, s15, v250
	v_med3_f32 v70, v70, s15, v250
	v_med3_f32 v71, v71, s15, v250
	v_cvt_pk_fp8_f32 v193, v68, v69
	v_cvt_pk_fp8_f32 v193, v70, v71 op_sel:[0,0,1]
	v_mul_f32_e32 v72, 0x42800000, v72
	v_mul_f32_e32 v73, 0x42800000, v73
	v_mul_f32_e32 v74, 0x42800000, v74
	v_mul_f32_e32 v75, 0x42800000, v75
	v_med3_f32 v72, v72, s15, v250
	v_med3_f32 v73, v73, s15, v250
	v_med3_f32 v74, v74, s15, v250
	v_med3_f32 v75, v75, s15, v250
	v_cvt_pk_fp8_f32 v194, v72, v73
	v_cvt_pk_fp8_f32 v194, v74, v75 op_sel:[0,0,1]
	v_mul_f32_e32 v76, 0x42800000, v76
	v_mul_f32_e32 v77, 0x42800000, v77
	v_mul_f32_e32 v78, 0x42800000, v78
	v_mul_f32_e32 v79, 0x42800000, v79
	v_med3_f32 v76, v76, s15, v250
	v_med3_f32 v77, v77, s15, v250
	v_med3_f32 v78, v78, s15, v250
	v_med3_f32 v79, v79, s15, v250
	v_cvt_pk_fp8_f32 v195, v76, v77
	v_cvt_pk_fp8_f32 v195, v78, v79 op_sel:[0,0,1]
	v_mul_f32_e32 v80, 0x42800000, v80
	v_mul_f32_e32 v81, 0x42800000, v81
	v_mul_f32_e32 v82, 0x42800000, v82
	v_mul_f32_e32 v83, 0x42800000, v83
	v_med3_f32 v80, v80, s15, v250
	v_med3_f32 v81, v81, s15, v250
	v_med3_f32 v82, v82, s15, v250
	v_med3_f32 v83, v83, s15, v250
	v_cvt_pk_fp8_f32 v196, v80, v81
	v_cvt_pk_fp8_f32 v196, v82, v83 op_sel:[0,0,1]
	v_mul_f32_e32 v84, 0x42800000, v84
	v_mul_f32_e32 v85, 0x42800000, v85
	v_mul_f32_e32 v86, 0x42800000, v86
	v_mul_f32_e32 v87, 0x42800000, v87
	v_med3_f32 v84, v84, s15, v250
	v_med3_f32 v85, v85, s15, v250
	v_med3_f32 v86, v86, s15, v250
	v_med3_f32 v87, v87, s15, v250
	v_cvt_pk_fp8_f32 v197, v84, v85
	v_cvt_pk_fp8_f32 v197, v86, v87 op_sel:[0,0,1]
	v_mul_f32_e32 v88, 0x42800000, v88
	v_mul_f32_e32 v89, 0x42800000, v89
	v_mul_f32_e32 v90, 0x42800000, v90
	v_mul_f32_e32 v91, 0x42800000, v91
	v_med3_f32 v88, v88, s15, v250
	v_med3_f32 v89, v89, s15, v250
	v_med3_f32 v90, v90, s15, v250
	v_med3_f32 v91, v91, s15, v250
	v_cvt_pk_fp8_f32 v198, v88, v89
	v_cvt_pk_fp8_f32 v198, v90, v91 op_sel:[0,0,1]
	v_mul_f32_e32 v92, 0x42800000, v92
	v_mul_f32_e32 v93, 0x42800000, v93
	v_mul_f32_e32 v94, 0x42800000, v94
	v_mul_f32_e32 v95, 0x42800000, v95
	v_med3_f32 v92, v92, s15, v250
	v_med3_f32 v93, v93, s15, v250
	v_med3_f32 v94, v94, s15, v250
	v_med3_f32 v95, v95, s15, v250
	v_cvt_pk_fp8_f32 v199, v92, v93
	v_cvt_pk_fp8_f32 v199, v94, v95 op_sel:[0,0,1]
	v_mul_f32_e32 v96, 0x42800000, v96
	v_mul_f32_e32 v97, 0x42800000, v97
	v_mul_f32_e32 v98, 0x42800000, v98
	v_mul_f32_e32 v99, 0x42800000, v99
	v_med3_f32 v96, v96, s15, v250
	v_med3_f32 v97, v97, s15, v250
	v_med3_f32 v98, v98, s15, v250
	v_med3_f32 v99, v99, s15, v250
	v_cvt_pk_fp8_f32 v200, v96, v97
	v_cvt_pk_fp8_f32 v200, v98, v99 op_sel:[0,0,1]
	v_mul_f32_e32 v100, 0x42800000, v100
	v_mul_f32_e32 v101, 0x42800000, v101
	v_mul_f32_e32 v102, 0x42800000, v102
	v_mul_f32_e32 v103, 0x42800000, v103
	v_med3_f32 v100, v100, s15, v250
	v_med3_f32 v101, v101, s15, v250
	v_med3_f32 v102, v102, s15, v250
	v_med3_f32 v103, v103, s15, v250
	v_cvt_pk_fp8_f32 v201, v100, v101
	v_cvt_pk_fp8_f32 v201, v102, v103 op_sel:[0,0,1]
	v_mul_f32_e32 v104, 0x42800000, v104
	v_mul_f32_e32 v105, 0x42800000, v105
	v_mul_f32_e32 v106, 0x42800000, v106
	v_mul_f32_e32 v107, 0x42800000, v107
	v_med3_f32 v104, v104, s15, v250
	v_med3_f32 v105, v105, s15, v250
	v_med3_f32 v106, v106, s15, v250
	v_med3_f32 v107, v107, s15, v250
	v_cvt_pk_fp8_f32 v202, v104, v105
	v_cvt_pk_fp8_f32 v202, v106, v107 op_sel:[0,0,1]
	v_mul_f32_e32 v108, 0x42800000, v108
	v_mul_f32_e32 v109, 0x42800000, v109
	v_mul_f32_e32 v110, 0x42800000, v110
	v_mul_f32_e32 v111, 0x42800000, v111
	v_med3_f32 v108, v108, s15, v250
	v_med3_f32 v109, v109, s15, v250
	v_med3_f32 v110, v110, s15, v250
	v_med3_f32 v111, v111, s15, v250
	v_cvt_pk_fp8_f32 v203, v108, v109
	v_cvt_pk_fp8_f32 v203, v110, v111 op_sel:[0,0,1]
	v_mul_f32_e32 v112, 0x42800000, v112
	v_mul_f32_e32 v113, 0x42800000, v113
	v_mul_f32_e32 v114, 0x42800000, v114
	v_mul_f32_e32 v115, 0x42800000, v115
	v_med3_f32 v112, v112, s15, v250
	v_med3_f32 v113, v113, s15, v250
	v_med3_f32 v114, v114, s15, v250
	v_med3_f32 v115, v115, s15, v250
	v_cvt_pk_fp8_f32 v204, v112, v113
	v_cvt_pk_fp8_f32 v204, v114, v115 op_sel:[0,0,1]
	v_mul_f32_e32 v116, 0x42800000, v116
	v_mul_f32_e32 v117, 0x42800000, v117
	v_mul_f32_e32 v118, 0x42800000, v118
	v_mul_f32_e32 v119, 0x42800000, v119
	v_med3_f32 v116, v116, s15, v250
	v_med3_f32 v117, v117, s15, v250
	v_med3_f32 v118, v118, s15, v250
	v_med3_f32 v119, v119, s15, v250
	v_cvt_pk_fp8_f32 v205, v116, v117
	v_cvt_pk_fp8_f32 v205, v118, v119 op_sel:[0,0,1]
	v_mul_f32_e32 v120, 0x42800000, v120
	v_mul_f32_e32 v121, 0x42800000, v121
	v_mul_f32_e32 v122, 0x42800000, v122
	v_mul_f32_e32 v123, 0x42800000, v123
	v_med3_f32 v120, v120, s15, v250
	v_med3_f32 v121, v121, s15, v250
	v_med3_f32 v122, v122, s15, v250
	v_med3_f32 v123, v123, s15, v250
	v_cvt_pk_fp8_f32 v206, v120, v121
	v_cvt_pk_fp8_f32 v206, v122, v123 op_sel:[0,0,1]
	v_mul_f32_e32 v124, 0x42800000, v124
	v_mul_f32_e32 v125, 0x42800000, v125
	v_mul_f32_e32 v126, 0x42800000, v126
	v_mul_f32_e32 v127, 0x42800000, v127
	v_med3_f32 v124, v124, s15, v250
	v_med3_f32 v125, v125, s15, v250
	v_med3_f32 v126, v126, s15, v250
	v_med3_f32 v127, v127, s15, v250
	v_cvt_pk_fp8_f32 v207, v124, v125
	v_cvt_pk_fp8_f32 v207, v126, v127 op_sel:[0,0,1]
	s_min_u32 s22, s2, s28
	s_cmp_lt_u32 s22, 0x10000
	s_cbranch_scc0 .Lcv_dn_4
	s_lshr_b32 s23, s22, 11
	s_bfe_u32 s24, s22, 0x40007
	s_and_b32 s25, s22, 0x7f
	s_lshl_b32 s30, s24, 7
	s_lshl_b32 s24, s24, 21
	s_lshl_b32 s22, s25, 7
	s_add_u32 s24, s24, s22
	s_lshl_b32 s25, s25, 16
	s_add_u32 s30, s30, s25
	s_lshl_b32 s22, s23, 25
	s_add_u32 s24, s24, s22
	s_add_u32 s4, s70, s24
	s_addc_u32 s5, s71, 0
	s_lshl_b32 s23, s23, 23
	s_add_u32 s30, s30, s23
	s_add_u32 s30, s30, 0x38ee1c00
	s_add_u32 s20, s92, s30
	s_addc_u32 s21, s93, 0
	s_mov_b32 s14, 0x20000
	s_mov_b64 vcc, -1
	s_branch .Lcv_ld_4

.Lcv_ld_4:
	s_add_u32 s2, s2, s3
	v_cndmask_b32_e32 v246, v245, v244, vcc
	global_load_dwordx4 v[64:67], v246, s[4:5] nt
	s_add_u32 s4, s4, s14
	s_addc_u32 s5, s5, 0
	global_load_dwordx4 v[68:71], v246, s[4:5] nt
	s_add_u32 s4, s4, s14
	s_addc_u32 s5, s5, 0
	global_load_dwordx4 v[72:75], v246, s[4:5] nt
	s_add_u32 s4, s4, s14
	s_addc_u32 s5, s5, 0
	global_load_dwordx4 v[76:79], v246, s[4:5] nt
	s_add_u32 s4, s4, s14
	s_addc_u32 s5, s5, 0
	global_load_dwordx4 v[80:83], v246, s[4:5] nt
	s_add_u32 s4, s4, s14
	s_addc_u32 s5, s5, 0
	global_load_dwordx4 v[84:87], v246, s[4:5] nt
	s_add_u32 s4, s4, s14
	s_addc_u32 s5, s5, 0
	global_load_dwordx4 v[88:91], v246, s[4:5] nt
	s_add_u32 s4, s4, s14
	s_addc_u32 s5, s5, 0
	global_load_dwordx4 v[92:95], v246, s[4:5] nt
	s_add_u32 s4, s4, s14
	s_addc_u32 s5, s5, 0
	global_load_dwordx4 v[96:99], v246, s[4:5] nt
	s_add_u32 s4, s4, s14
	s_addc_u32 s5, s5, 0
	global_load_dwordx4 v[100:103], v246, s[4:5] nt
	s_add_u32 s4, s4, s14
	s_addc_u32 s5, s5, 0
	global_load_dwordx4 v[104:107], v246, s[4:5] nt
	s_add_u32 s4, s4, s14
	s_addc_u32 s5, s5, 0
	global_load_dwordx4 v[108:111], v246, s[4:5] nt
	s_add_u32 s4, s4, s14
	s_addc_u32 s5, s5, 0
	global_load_dwordx4 v[112:115], v246, s[4:5] nt
	s_add_u32 s4, s4, s14
	s_addc_u32 s5, s5, 0
	global_load_dwordx4 v[116:119], v246, s[4:5] nt
	s_add_u32 s4, s4, s14
	s_addc_u32 s5, s5, 0
	global_load_dwordx4 v[120:123], v246, s[4:5] nt
	s_add_u32 s4, s4, s14
	s_addc_u32 s5, s5, 0
	global_load_dwordx4 v[124:127], v246, s[4:5] nt
	ds_write_b32 v247, v192 offset:0
	ds_write_b32 v247, v193 offset:32
	ds_write_b32 v247, v194 offset:64
	ds_write_b32 v247, v195 offset:96
	ds_write_b32 v247, v196 offset:128
	ds_write_b32 v247, v197 offset:160
	ds_write_b32 v247, v198 offset:192
	ds_write_b32 v247, v199 offset:224
	ds_write_b32 v247, v200 offset:256
	ds_write_b32 v247, v201 offset:288
	ds_write_b32 v247, v202 offset:320
	ds_write_b32 v247, v203 offset:352
	ds_write_b32 v247, v204 offset:384
	ds_write_b32 v247, v205 offset:416
	ds_write_b32 v247, v206 offset:448
	ds_write_b32 v247, v207 offset:480
	ds_read_b128 v[208:211], v248 offset:0
	ds_read_b128 v[212:215], v248 offset:16
	ds_read_b128 v[216:219], v248 offset:32
	ds_read_b128 v[220:223], v248 offset:48
	s_waitcnt lgkmcnt(3)
	v_perm_b32 v240, v209, v208, s16
	v_perm_b32 v241, v209, v208, s17
	v_perm_b32 v242, v211, v210, s16
	v_perm_b32 v243, v211, v210, s17
	v_perm_b32 v224, v242, v240, s18
	v_perm_b32 v228, v242, v240, s19
	v_perm_b32 v232, v243, v241, s18
	v_perm_b32 v236, v243, v241, s19
	s_waitcnt lgkmcnt(2)
	v_perm_b32 v240, v213, v212, s16
	v_perm_b32 v241, v213, v212, s17
	v_perm_b32 v242, v215, v214, s16
	v_perm_b32 v243, v215, v214, s17
	v_perm_b32 v225, v242, v240, s18
	v_perm_b32 v229, v242, v240, s19
	v_perm_b32 v233, v243, v241, s18
	v_perm_b32 v237, v243, v241, s19
	s_waitcnt lgkmcnt(1)
	v_perm_b32 v240, v217, v216, s16
	v_perm_b32 v241, v217, v216, s17
	v_perm_b32 v242, v219, v218, s16
	v_perm_b32 v243, v219, v218, s17
	v_perm_b32 v226, v242, v240, s18
	v_perm_b32 v230, v242, v240, s19
	v_perm_b32 v234, v243, v241, s18
	v_perm_b32 v238, v243, v241, s19
	s_waitcnt lgkmcnt(0)
	v_perm_b32 v240, v221, v220, s16
	v_perm_b32 v241, v221, v220, s17
	v_perm_b32 v242, v223, v222, s16
	v_perm_b32 v243, v223, v222, s17
	v_perm_b32 v227, v242, v240, s18
	v_perm_b32 v231, v242, v240, s19
	v_perm_b32 v235, v243, v241, s18
	v_perm_b32 v239, v243, v241, s19
	s_add_u32 s26, s8, 0x1000
	s_addc_u32 s27, s9, 0
	global_store_dwordx4 v249, v[224:227], s[8:9]
	global_store_dwordx4 v249, v[228:231], s[8:9] offset:2048
	global_store_dwordx4 v249, v[232:235], s[26:27]
	global_store_dwordx4 v249, v[236:239], s[26:27] offset:2048
	s_mov_b64 s[8:9], s[20:21]
	s_waitcnt vmcnt(40)
	v_mul_f32_e32 v128, 0x42800000, v128
	v_mul_f32_e32 v129, 0x42800000, v129
	v_mul_f32_e32 v130, 0x42800000, v130
	v_mul_f32_e32 v131, 0x42800000, v131
	v_med3_f32 v128, v128, s15, v250
	v_med3_f32 v129, v129, s15, v250
	v_med3_f32 v130, v130, s15, v250
	v_med3_f32 v131, v131, s15, v250
	v_cvt_pk_fp8_f32 v192, v128, v129
	v_cvt_pk_fp8_f32 v192, v130, v131 op_sel:[0,0,1]
	v_mul_f32_e32 v132, 0x42800000, v132
	v_mul_f32_e32 v133, 0x42800000, v133
	v_mul_f32_e32 v134, 0x42800000, v134
	v_mul_f32_e32 v135, 0x42800000, v135
	v_med3_f32 v132, v132, s15, v250
	v_med3_f32 v133, v133, s15, v250
	v_med3_f32 v134, v134, s15, v250
	v_med3_f32 v135, v135, s15, v250
	v_cvt_pk_fp8_f32 v193, v132, v133
	v_cvt_pk_fp8_f32 v193, v134, v135 op_sel:[0,0,1]
	v_mul_f32_e32 v136, 0x42800000, v136
	v_mul_f32_e32 v137, 0x42800000, v137
	v_mul_f32_e32 v138, 0x42800000, v138
	v_mul_f32_e32 v139, 0x42800000, v139
	v_med3_f32 v136, v136, s15, v250
	v_med3_f32 v137, v137, s15, v250
	v_med3_f32 v138, v138, s15, v250
	v_med3_f32 v139, v139, s15, v250
	v_cvt_pk_fp8_f32 v194, v136, v137
	v_cvt_pk_fp8_f32 v194, v138, v139 op_sel:[0,0,1]
	v_mul_f32_e32 v140, 0x42800000, v140
	v_mul_f32_e32 v141, 0x42800000, v141
	v_mul_f32_e32 v142, 0x42800000, v142
	v_mul_f32_e32 v143, 0x42800000, v143
	v_med3_f32 v140, v140, s15, v250
	v_med3_f32 v141, v141, s15, v250
	v_med3_f32 v142, v142, s15, v250
	v_med3_f32 v143, v143, s15, v250
	v_cvt_pk_fp8_f32 v195, v140, v141
	v_cvt_pk_fp8_f32 v195, v142, v143 op_sel:[0,0,1]
	v_mul_f32_e32 v144, 0x42800000, v144
	v_mul_f32_e32 v145, 0x42800000, v145
	v_mul_f32_e32 v146, 0x42800000, v146
	v_mul_f32_e32 v147, 0x42800000, v147
	v_med3_f32 v144, v144, s15, v250
	v_med3_f32 v145, v145, s15, v250
	v_med3_f32 v146, v146, s15, v250
	v_med3_f32 v147, v147, s15, v250
	v_cvt_pk_fp8_f32 v196, v144, v145
	v_cvt_pk_fp8_f32 v196, v146, v147 op_sel:[0,0,1]
	v_mul_f32_e32 v148, 0x42800000, v148
	v_mul_f32_e32 v149, 0x42800000, v149
	v_mul_f32_e32 v150, 0x42800000, v150
	v_mul_f32_e32 v151, 0x42800000, v151
	v_med3_f32 v148, v148, s15, v250
	v_med3_f32 v149, v149, s15, v250
	v_med3_f32 v150, v150, s15, v250
	v_med3_f32 v151, v151, s15, v250
	v_cvt_pk_fp8_f32 v197, v148, v149
	v_cvt_pk_fp8_f32 v197, v150, v151 op_sel:[0,0,1]
	v_mul_f32_e32 v152, 0x42800000, v152
	v_mul_f32_e32 v153, 0x42800000, v153
	v_mul_f32_e32 v154, 0x42800000, v154
	v_mul_f32_e32 v155, 0x42800000, v155
	v_med3_f32 v152, v152, s15, v250
	v_med3_f32 v153, v153, s15, v250
	v_med3_f32 v154, v154, s15, v250
	v_med3_f32 v155, v155, s15, v250
	v_cvt_pk_fp8_f32 v198, v152, v153
	v_cvt_pk_fp8_f32 v198, v154, v155 op_sel:[0,0,1]
	v_mul_f32_e32 v156, 0x42800000, v156
	v_mul_f32_e32 v157, 0x42800000, v157
	v_mul_f32_e32 v158, 0x42800000, v158
	v_mul_f32_e32 v159, 0x42800000, v159
	v_med3_f32 v156, v156, s15, v250
	v_med3_f32 v157, v157, s15, v250
	v_med3_f32 v158, v158, s15, v250
	v_med3_f32 v159, v159, s15, v250
	v_cvt_pk_fp8_f32 v199, v156, v157
	v_cvt_pk_fp8_f32 v199, v158, v159 op_sel:[0,0,1]
	v_mul_f32_e32 v160, 0x42800000, v160
	v_mul_f32_e32 v161, 0x42800000, v161
	v_mul_f32_e32 v162, 0x42800000, v162
	v_mul_f32_e32 v163, 0x42800000, v163
	v_med3_f32 v160, v160, s15, v250
	v_med3_f32 v161, v161, s15, v250
	v_med3_f32 v162, v162, s15, v250
	v_med3_f32 v163, v163, s15, v250
	v_cvt_pk_fp8_f32 v200, v160, v161
	v_cvt_pk_fp8_f32 v200, v162, v163 op_sel:[0,0,1]
	v_mul_f32_e32 v164, 0x42800000, v164
	v_mul_f32_e32 v165, 0x42800000, v165
	v_mul_f32_e32 v166, 0x42800000, v166
	v_mul_f32_e32 v167, 0x42800000, v167
	v_med3_f32 v164, v164, s15, v250
	v_med3_f32 v165, v165, s15, v250
	v_med3_f32 v166, v166, s15, v250
	v_med3_f32 v167, v167, s15, v250
	v_cvt_pk_fp8_f32 v201, v164, v165
	v_cvt_pk_fp8_f32 v201, v166, v167 op_sel:[0,0,1]
	v_mul_f32_e32 v168, 0x42800000, v168
	v_mul_f32_e32 v169, 0x42800000, v169
	v_mul_f32_e32 v170, 0x42800000, v170
	v_mul_f32_e32 v171, 0x42800000, v171
	v_med3_f32 v168, v168, s15, v250
	v_med3_f32 v169, v169, s15, v250
	v_med3_f32 v170, v170, s15, v250
	v_med3_f32 v171, v171, s15, v250
	v_cvt_pk_fp8_f32 v202, v168, v169
	v_cvt_pk_fp8_f32 v202, v170, v171 op_sel:[0,0,1]
	v_mul_f32_e32 v172, 0x42800000, v172
	v_mul_f32_e32 v173, 0x42800000, v173
	v_mul_f32_e32 v174, 0x42800000, v174
	v_mul_f32_e32 v175, 0x42800000, v175
	v_med3_f32 v172, v172, s15, v250
	v_med3_f32 v173, v173, s15, v250
	v_med3_f32 v174, v174, s15, v250
	v_med3_f32 v175, v175, s15, v250
	v_cvt_pk_fp8_f32 v203, v172, v173
	v_cvt_pk_fp8_f32 v203, v174, v175 op_sel:[0,0,1]
	v_mul_f32_e32 v176, 0x42800000, v176
	v_mul_f32_e32 v177, 0x42800000, v177
	v_mul_f32_e32 v178, 0x42800000, v178
	v_mul_f32_e32 v179, 0x42800000, v179
	v_med3_f32 v176, v176, s15, v250
	v_med3_f32 v177, v177, s15, v250
	v_med3_f32 v178, v178, s15, v250
	v_med3_f32 v179, v179, s15, v250
	v_cvt_pk_fp8_f32 v204, v176, v177
	v_cvt_pk_fp8_f32 v204, v178, v179 op_sel:[0,0,1]
	v_mul_f32_e32 v180, 0x42800000, v180
	v_mul_f32_e32 v181, 0x42800000, v181
	v_mul_f32_e32 v182, 0x42800000, v182
	v_mul_f32_e32 v183, 0x42800000, v183
	v_med3_f32 v180, v180, s15, v250
	v_med3_f32 v181, v181, s15, v250
	v_med3_f32 v182, v182, s15, v250
	v_med3_f32 v183, v183, s15, v250
	v_cvt_pk_fp8_f32 v205, v180, v181
	v_cvt_pk_fp8_f32 v205, v182, v183 op_sel:[0,0,1]
	v_mul_f32_e32 v184, 0x42800000, v184
	v_mul_f32_e32 v185, 0x42800000, v185
	v_mul_f32_e32 v186, 0x42800000, v186
	v_mul_f32_e32 v187, 0x42800000, v187
	v_med3_f32 v184, v184, s15, v250
	v_med3_f32 v185, v185, s15, v250
	v_med3_f32 v186, v186, s15, v250
	v_med3_f32 v187, v187, s15, v250
	v_cvt_pk_fp8_f32 v206, v184, v185
	v_cvt_pk_fp8_f32 v206, v186, v187 op_sel:[0,0,1]
	v_mul_f32_e32 v188, 0x42800000, v188
	v_mul_f32_e32 v189, 0x42800000, v189
	v_mul_f32_e32 v190, 0x42800000, v190
	v_mul_f32_e32 v191, 0x42800000, v191
	v_med3_f32 v188, v188, s15, v250
	v_med3_f32 v189, v189, s15, v250
	v_med3_f32 v190, v190, s15, v250
	v_med3_f32 v191, v191, s15, v250
	v_cvt_pk_fp8_f32 v207, v188, v189
	v_cvt_pk_fp8_f32 v207, v190, v191 op_sel:[0,0,1]
	s_min_u32 s22, s2, s28
	s_cmp_lt_u32 s22, 0x10000
	s_cbranch_scc0 .Lcv_dn_5
	s_lshr_b32 s23, s22, 11
	s_bfe_u32 s24, s22, 0x40007
	s_and_b32 s25, s22, 0x7f
	s_lshl_b32 s30, s24, 7
	s_lshl_b32 s24, s24, 21
	s_lshl_b32 s22, s25, 7
	s_add_u32 s24, s24, s22
	s_lshl_b32 s25, s25, 16
	s_add_u32 s30, s30, s25
	s_lshl_b32 s22, s23, 25
	s_add_u32 s24, s24, s22
	s_add_u32 s4, s70, s24
	s_addc_u32 s5, s71, 0
	s_lshl_b32 s23, s23, 23
	s_add_u32 s30, s30, s23
	s_add_u32 s30, s30, 0x38ee1c00
	s_add_u32 s20, s92, s30
	s_addc_u32 s21, s93, 0
	s_mov_b32 s14, 0x20000
	s_mov_b64 vcc, -1
	s_branch .Lcv_ld_5

.Lcv_ld_5:
	s_add_u32 s2, s2, s3
	v_cndmask_b32_e32 v246, v245, v244, vcc
	global_load_dwordx4 v[128:131], v246, s[4:5] nt
	s_add_u32 s4, s4, s14
	s_addc_u32 s5, s5, 0
	global_load_dwordx4 v[132:135], v246, s[4:5] nt
	s_add_u32 s4, s4, s14
	s_addc_u32 s5, s5, 0
	global_load_dwordx4 v[136:139], v246, s[4:5] nt
	s_add_u32 s4, s4, s14
	s_addc_u32 s5, s5, 0
	global_load_dwordx4 v[140:143], v246, s[4:5] nt
	s_add_u32 s4, s4, s14
	s_addc_u32 s5, s5, 0
	global_load_dwordx4 v[144:147], v246, s[4:5] nt
	s_add_u32 s4, s4, s14
	s_addc_u32 s5, s5, 0
	global_load_dwordx4 v[148:151], v246, s[4:5] nt
	s_add_u32 s4, s4, s14
	s_addc_u32 s5, s5, 0
	global_load_dwordx4 v[152:155], v246, s[4:5] nt
	s_add_u32 s4, s4, s14
	s_addc_u32 s5, s5, 0
	global_load_dwordx4 v[156:159], v246, s[4:5] nt
	s_add_u32 s4, s4, s14
	s_addc_u32 s5, s5, 0
	global_load_dwordx4 v[160:163], v246, s[4:5] nt
	s_add_u32 s4, s4, s14
	s_addc_u32 s5, s5, 0
	global_load_dwordx4 v[164:167], v246, s[4:5] nt
	s_add_u32 s4, s4, s14
	s_addc_u32 s5, s5, 0
	global_load_dwordx4 v[168:171], v246, s[4:5] nt
	s_add_u32 s4, s4, s14
	s_addc_u32 s5, s5, 0
	global_load_dwordx4 v[172:175], v246, s[4:5] nt
	s_add_u32 s4, s4, s14
	s_addc_u32 s5, s5, 0
	global_load_dwordx4 v[176:179], v246, s[4:5] nt
	s_add_u32 s4, s4, s14
	s_addc_u32 s5, s5, 0
	global_load_dwordx4 v[180:183], v246, s[4:5] nt
	s_add_u32 s4, s4, s14
	s_addc_u32 s5, s5, 0
	global_load_dwordx4 v[184:187], v246, s[4:5] nt
	s_add_u32 s4, s4, s14
	s_addc_u32 s5, s5, 0
	global_load_dwordx4 v[188:191], v246, s[4:5] nt
	ds_write_b32 v247, v192 offset:0
	ds_write_b32 v247, v193 offset:32
	ds_write_b32 v247, v194 offset:64
	ds_write_b32 v247, v195 offset:96
	ds_write_b32 v247, v196 offset:128
	ds_write_b32 v247, v197 offset:160
	ds_write_b32 v247, v198 offset:192
	ds_write_b32 v247, v199 offset:224
	ds_write_b32 v247, v200 offset:256
	ds_write_b32 v247, v201 offset:288
	ds_write_b32 v247, v202 offset:320
	ds_write_b32 v247, v203 offset:352
	ds_write_b32 v247, v204 offset:384
	ds_write_b32 v247, v205 offset:416
	ds_write_b32 v247, v206 offset:448
	ds_write_b32 v247, v207 offset:480
	ds_read_b128 v[208:211], v248 offset:0
	ds_read_b128 v[212:215], v248 offset:16
	ds_read_b128 v[216:219], v248 offset:32
	ds_read_b128 v[220:223], v248 offset:48
	s_waitcnt lgkmcnt(3)
	v_perm_b32 v240, v209, v208, s16
	v_perm_b32 v241, v209, v208, s17
	v_perm_b32 v242, v211, v210, s16
	v_perm_b32 v243, v211, v210, s17
	v_perm_b32 v224, v242, v240, s18
	v_perm_b32 v228, v242, v240, s19
	v_perm_b32 v232, v243, v241, s18
	v_perm_b32 v236, v243, v241, s19
	s_waitcnt lgkmcnt(2)
	v_perm_b32 v240, v213, v212, s16
	v_perm_b32 v241, v213, v212, s17
	v_perm_b32 v242, v215, v214, s16
	v_perm_b32 v243, v215, v214, s17
	v_perm_b32 v225, v242, v240, s18
	v_perm_b32 v229, v242, v240, s19
	v_perm_b32 v233, v243, v241, s18
	v_perm_b32 v237, v243, v241, s19
	s_waitcnt lgkmcnt(1)
	v_perm_b32 v240, v217, v216, s16
	v_perm_b32 v241, v217, v216, s17
	v_perm_b32 v242, v219, v218, s16
	v_perm_b32 v243, v219, v218, s17
	v_perm_b32 v226, v242, v240, s18
	v_perm_b32 v230, v242, v240, s19
	v_perm_b32 v234, v243, v241, s18
	v_perm_b32 v238, v243, v241, s19
	s_waitcnt lgkmcnt(0)
	v_perm_b32 v240, v221, v220, s16
	v_perm_b32 v241, v221, v220, s17
	v_perm_b32 v242, v223, v222, s16
	v_perm_b32 v243, v223, v222, s17
	v_perm_b32 v227, v242, v240, s18
	v_perm_b32 v231, v242, v240, s19
	v_perm_b32 v235, v243, v241, s18
	v_perm_b32 v239, v243, v241, s19
	s_add_u32 s26, s10, 0x1000
	s_addc_u32 s27, s11, 0
	global_store_dwordx4 v249, v[224:227], s[10:11]
	global_store_dwordx4 v249, v[228:231], s[10:11] offset:2048
	global_store_dwordx4 v249, v[232:235], s[26:27]
	global_store_dwordx4 v249, v[236:239], s[26:27] offset:2048
	s_mov_b64 s[10:11], s[20:21]
	s_sub_u32 s22, s2, s31
	s_cmp_gt_u32 s22, s28
	s_cbranch_scc1 .Lcv_done
.Lcv_loop:
	s_waitcnt vmcnt(44)
	v_mul_f32_e32 v0, 0x42800000, v0
	v_mul_f32_e32 v1, 0x42800000, v1
	v_mul_f32_e32 v2, 0x42800000, v2
	v_mul_f32_e32 v3, 0x42800000, v3
	v_med3_f32 v0, v0, s15, v250
	v_med3_f32 v1, v1, s15, v250
	v_med3_f32 v2, v2, s15, v250
	v_med3_f32 v3, v3, s15, v250
	v_cvt_pk_fp8_f32 v192, v0, v1
	v_cvt_pk_fp8_f32 v192, v2, v3 op_sel:[0,0,1]
	v_mul_f32_e32 v4, 0x42800000, v4
	v_mul_f32_e32 v5, 0x42800000, v5
	v_mul_f32_e32 v6, 0x42800000, v6
	v_mul_f32_e32 v7, 0x42800000, v7
	v_med3_f32 v4, v4, s15, v250
	v_med3_f32 v5, v5, s15, v250
	v_med3_f32 v6, v6, s15, v250
	v_med3_f32 v7, v7, s15, v250
	v_cvt_pk_fp8_f32 v193, v4, v5
	v_cvt_pk_fp8_f32 v193, v6, v7 op_sel:[0,0,1]
	v_mul_f32_e32 v8, 0x42800000, v8
	v_mul_f32_e32 v9, 0x42800000, v9
	v_mul_f32_e32 v10, 0x42800000, v10
	v_mul_f32_e32 v11, 0x42800000, v11
	v_med3_f32 v8, v8, s15, v250
	v_med3_f32 v9, v9, s15, v250
	v_med3_f32 v10, v10, s15, v250
	v_med3_f32 v11, v11, s15, v250
	v_cvt_pk_fp8_f32 v194, v8, v9
	v_cvt_pk_fp8_f32 v194, v10, v11 op_sel:[0,0,1]
	v_mul_f32_e32 v12, 0x42800000, v12
	v_mul_f32_e32 v13, 0x42800000, v13
	v_mul_f32_e32 v14, 0x42800000, v14
	v_mul_f32_e32 v15, 0x42800000, v15
	v_med3_f32 v12, v12, s15, v250
	v_med3_f32 v13, v13, s15, v250
	v_med3_f32 v14, v14, s15, v250
	v_med3_f32 v15, v15, s15, v250
	v_cvt_pk_fp8_f32 v195, v12, v13
	v_cvt_pk_fp8_f32 v195, v14, v15 op_sel:[0,0,1]
	v_mul_f32_e32 v16, 0x42800000, v16
	v_mul_f32_e32 v17, 0x42800000, v17
	v_mul_f32_e32 v18, 0x42800000, v18
	v_mul_f32_e32 v19, 0x42800000, v19
	v_med3_f32 v16, v16, s15, v250
	v_med3_f32 v17, v17, s15, v250
	v_med3_f32 v18, v18, s15, v250
	v_med3_f32 v19, v19, s15, v250
	v_cvt_pk_fp8_f32 v196, v16, v17
	v_cvt_pk_fp8_f32 v196, v18, v19 op_sel:[0,0,1]
	v_mul_f32_e32 v20, 0x42800000, v20
	v_mul_f32_e32 v21, 0x42800000, v21
	v_mul_f32_e32 v22, 0x42800000, v22
	v_mul_f32_e32 v23, 0x42800000, v23
	v_med3_f32 v20, v20, s15, v250
	v_med3_f32 v21, v21, s15, v250
	v_med3_f32 v22, v22, s15, v250
	v_med3_f32 v23, v23, s15, v250
	v_cvt_pk_fp8_f32 v197, v20, v21
	v_cvt_pk_fp8_f32 v197, v22, v23 op_sel:[0,0,1]
	v_mul_f32_e32 v24, 0x42800000, v24
	v_mul_f32_e32 v25, 0x42800000, v25
	v_mul_f32_e32 v26, 0x42800000, v26
	v_mul_f32_e32 v27, 0x42800000, v27
	v_med3_f32 v24, v24, s15, v250
	v_med3_f32 v25, v25, s15, v250
	v_med3_f32 v26, v26, s15, v250
	v_med3_f32 v27, v27, s15, v250
	v_cvt_pk_fp8_f32 v198, v24, v25
	v_cvt_pk_fp8_f32 v198, v26, v27 op_sel:[0,0,1]
	v_mul_f32_e32 v28, 0x42800000, v28
	v_mul_f32_e32 v29, 0x42800000, v29
	v_mul_f32_e32 v30, 0x42800000, v30
	v_mul_f32_e32 v31, 0x42800000, v31
	v_med3_f32 v28, v28, s15, v250
	v_med3_f32 v29, v29, s15, v250
	v_med3_f32 v30, v30, s15, v250
	v_med3_f32 v31, v31, s15, v250
	v_cvt_pk_fp8_f32 v199, v28, v29
	v_cvt_pk_fp8_f32 v199, v30, v31 op_sel:[0,0,1]
	v_mul_f32_e32 v32, 0x42800000, v32
	v_mul_f32_e32 v33, 0x42800000, v33
	v_mul_f32_e32 v34, 0x42800000, v34
	v_mul_f32_e32 v35, 0x42800000, v35
	v_med3_f32 v32, v32, s15, v250
	v_med3_f32 v33, v33, s15, v250
	v_med3_f32 v34, v34, s15, v250
	v_med3_f32 v35, v35, s15, v250
	v_cvt_pk_fp8_f32 v200, v32, v33
	v_cvt_pk_fp8_f32 v200, v34, v35 op_sel:[0,0,1]
	v_mul_f32_e32 v36, 0x42800000, v36
	v_mul_f32_e32 v37, 0x42800000, v37
	v_mul_f32_e32 v38, 0x42800000, v38
	v_mul_f32_e32 v39, 0x42800000, v39
	v_med3_f32 v36, v36, s15, v250
	v_med3_f32 v37, v37, s15, v250
	v_med3_f32 v38, v38, s15, v250
	v_med3_f32 v39, v39, s15, v250
	v_cvt_pk_fp8_f32 v201, v36, v37
	v_cvt_pk_fp8_f32 v201, v38, v39 op_sel:[0,0,1]
	v_mul_f32_e32 v40, 0x42800000, v40
	v_mul_f32_e32 v41, 0x42800000, v41
	v_mul_f32_e32 v42, 0x42800000, v42
	v_mul_f32_e32 v43, 0x42800000, v43
	v_med3_f32 v40, v40, s15, v250
	v_med3_f32 v41, v41, s15, v250
	v_med3_f32 v42, v42, s15, v250
	v_med3_f32 v43, v43, s15, v250
	v_cvt_pk_fp8_f32 v202, v40, v41
	v_cvt_pk_fp8_f32 v202, v42, v43 op_sel:[0,0,1]
	v_mul_f32_e32 v44, 0x42800000, v44
	v_mul_f32_e32 v45, 0x42800000, v45
	v_mul_f32_e32 v46, 0x42800000, v46
	v_mul_f32_e32 v47, 0x42800000, v47
	v_med3_f32 v44, v44, s15, v250
	v_med3_f32 v45, v45, s15, v250
	v_med3_f32 v46, v46, s15, v250
	v_med3_f32 v47, v47, s15, v250
	v_cvt_pk_fp8_f32 v203, v44, v45
	v_cvt_pk_fp8_f32 v203, v46, v47 op_sel:[0,0,1]
	v_mul_f32_e32 v48, 0x42800000, v48
	v_mul_f32_e32 v49, 0x42800000, v49
	v_mul_f32_e32 v50, 0x42800000, v50
	v_mul_f32_e32 v51, 0x42800000, v51
	v_med3_f32 v48, v48, s15, v250
	v_med3_f32 v49, v49, s15, v250
	v_med3_f32 v50, v50, s15, v250
	v_med3_f32 v51, v51, s15, v250
	v_cvt_pk_fp8_f32 v204, v48, v49
	v_cvt_pk_fp8_f32 v204, v50, v51 op_sel:[0,0,1]
	v_mul_f32_e32 v52, 0x42800000, v52
	v_mul_f32_e32 v53, 0x42800000, v53
	v_mul_f32_e32 v54, 0x42800000, v54
	v_mul_f32_e32 v55, 0x42800000, v55
	v_med3_f32 v52, v52, s15, v250
	v_med3_f32 v53, v53, s15, v250
	v_med3_f32 v54, v54, s15, v250
	v_med3_f32 v55, v55, s15, v250
	v_cvt_pk_fp8_f32 v205, v52, v53
	v_cvt_pk_fp8_f32 v205, v54, v55 op_sel:[0,0,1]
	v_mul_f32_e32 v56, 0x42800000, v56
	v_mul_f32_e32 v57, 0x42800000, v57
	v_mul_f32_e32 v58, 0x42800000, v58
	v_mul_f32_e32 v59, 0x42800000, v59
	v_med3_f32 v56, v56, s15, v250
	v_med3_f32 v57, v57, s15, v250
	v_med3_f32 v58, v58, s15, v250
	v_med3_f32 v59, v59, s15, v250
	v_cvt_pk_fp8_f32 v206, v56, v57
	v_cvt_pk_fp8_f32 v206, v58, v59 op_sel:[0,0,1]
	v_mul_f32_e32 v60, 0x42800000, v60
	v_mul_f32_e32 v61, 0x42800000, v61
	v_mul_f32_e32 v62, 0x42800000, v62
	v_mul_f32_e32 v63, 0x42800000, v63
	v_med3_f32 v60, v60, s15, v250
	v_med3_f32 v61, v61, s15, v250
	v_med3_f32 v62, v62, s15, v250
	v_med3_f32 v63, v63, s15, v250
	v_cvt_pk_fp8_f32 v207, v60, v61
	v_cvt_pk_fp8_f32 v207, v62, v63 op_sel:[0,0,1]
	s_min_u32 s22, s2, s28
	s_cmp_lt_u32 s22, 0x10000
	s_cbranch_scc0 .Lcv_dn_6
	s_lshr_b32 s23, s22, 11
	s_bfe_u32 s24, s22, 0x40007
	s_and_b32 s25, s22, 0x7f
	s_lshl_b32 s30, s24, 7
	s_lshl_b32 s24, s24, 21
	s_lshl_b32 s22, s25, 7
	s_add_u32 s24, s24, s22
	s_lshl_b32 s25, s25, 16
	s_add_u32 s30, s30, s25
	s_lshl_b32 s22, s23, 25
	s_add_u32 s24, s24, s22
	s_add_u32 s4, s70, s24
	s_addc_u32 s5, s71, 0
	s_lshl_b32 s23, s23, 23
	s_add_u32 s30, s30, s23
	s_add_u32 s30, s30, 0x38ee1c00
	s_add_u32 s20, s92, s30
	s_addc_u32 s21, s93, 0
	s_mov_b32 s14, 0x20000
	s_mov_b64 vcc, -1
	s_branch .Lcv_ld_6

.Lcv_ld_6:
	s_add_u32 s2, s2, s3
	v_cndmask_b32_e32 v246, v245, v244, vcc
	global_load_dwordx4 v[0:3], v246, s[4:5] nt
	s_add_u32 s4, s4, s14
	s_addc_u32 s5, s5, 0
	global_load_dwordx4 v[4:7], v246, s[4:5] nt
	s_add_u32 s4, s4, s14
	s_addc_u32 s5, s5, 0
	global_load_dwordx4 v[8:11], v246, s[4:5] nt
	s_add_u32 s4, s4, s14
	s_addc_u32 s5, s5, 0
	global_load_dwordx4 v[12:15], v246, s[4:5] nt
	s_add_u32 s4, s4, s14
	s_addc_u32 s5, s5, 0
	global_load_dwordx4 v[16:19], v246, s[4:5] nt
	s_add_u32 s4, s4, s14
	s_addc_u32 s5, s5, 0
	global_load_dwordx4 v[20:23], v246, s[4:5] nt
	s_add_u32 s4, s4, s14
	s_addc_u32 s5, s5, 0
	global_load_dwordx4 v[24:27], v246, s[4:5] nt
	s_add_u32 s4, s4, s14
	s_addc_u32 s5, s5, 0
	global_load_dwordx4 v[28:31], v246, s[4:5] nt
	s_add_u32 s4, s4, s14
	s_addc_u32 s5, s5, 0
	global_load_dwordx4 v[32:35], v246, s[4:5] nt
	s_add_u32 s4, s4, s14
	s_addc_u32 s5, s5, 0
	global_load_dwordx4 v[36:39], v246, s[4:5] nt
	s_add_u32 s4, s4, s14
	s_addc_u32 s5, s5, 0
	global_load_dwordx4 v[40:43], v246, s[4:5] nt
	s_add_u32 s4, s4, s14
	s_addc_u32 s5, s5, 0
	global_load_dwordx4 v[44:47], v246, s[4:5] nt
	s_add_u32 s4, s4, s14
	s_addc_u32 s5, s5, 0
	global_load_dwordx4 v[48:51], v246, s[4:5] nt
	s_add_u32 s4, s4, s14
	s_addc_u32 s5, s5, 0
	global_load_dwordx4 v[52:55], v246, s[4:5] nt
	s_add_u32 s4, s4, s14
	s_addc_u32 s5, s5, 0
	global_load_dwordx4 v[56:59], v246, s[4:5] nt
	s_add_u32 s4, s4, s14
	s_addc_u32 s5, s5, 0
	global_load_dwordx4 v[60:63], v246, s[4:5] nt
	ds_write_b32 v247, v192 offset:0
	ds_write_b32 v247, v193 offset:32
	ds_write_b32 v247, v194 offset:64
	ds_write_b32 v247, v195 offset:96
	ds_write_b32 v247, v196 offset:128
	ds_write_b32 v247, v197 offset:160
	ds_write_b32 v247, v198 offset:192
	ds_write_b32 v247, v199 offset:224
	ds_write_b32 v247, v200 offset:256
	ds_write_b32 v247, v201 offset:288
	ds_write_b32 v247, v202 offset:320
	ds_write_b32 v247, v203 offset:352
	ds_write_b32 v247, v204 offset:384
	ds_write_b32 v247, v205 offset:416
	ds_write_b32 v247, v206 offset:448
	ds_write_b32 v247, v207 offset:480
	ds_read_b128 v[208:211], v248 offset:0
	ds_read_b128 v[212:215], v248 offset:16
	ds_read_b128 v[216:219], v248 offset:32
	ds_read_b128 v[220:223], v248 offset:48
	s_waitcnt lgkmcnt(3)
	v_perm_b32 v240, v209, v208, s16
	v_perm_b32 v241, v209, v208, s17
	v_perm_b32 v242, v211, v210, s16
	v_perm_b32 v243, v211, v210, s17
	v_perm_b32 v224, v242, v240, s18
	v_perm_b32 v228, v242, v240, s19
	v_perm_b32 v232, v243, v241, s18
	v_perm_b32 v236, v243, v241, s19
	s_waitcnt lgkmcnt(2)
	v_perm_b32 v240, v213, v212, s16
	v_perm_b32 v241, v213, v212, s17
	v_perm_b32 v242, v215, v214, s16
	v_perm_b32 v243, v215, v214, s17
	v_perm_b32 v225, v242, v240, s18
	v_perm_b32 v229, v242, v240, s19
	v_perm_b32 v233, v243, v241, s18
	v_perm_b32 v237, v243, v241, s19
	s_waitcnt lgkmcnt(1)
	v_perm_b32 v240, v217, v216, s16
	v_perm_b32 v241, v217, v216, s17
	v_perm_b32 v242, v219, v218, s16
	v_perm_b32 v243, v219, v218, s17
	v_perm_b32 v226, v242, v240, s18
	v_perm_b32 v230, v242, v240, s19
	v_perm_b32 v234, v243, v241, s18
	v_perm_b32 v238, v243, v241, s19
	s_waitcnt lgkmcnt(0)
	v_perm_b32 v240, v221, v220, s16
	v_perm_b32 v241, v221, v220, s17
	v_perm_b32 v242, v223, v222, s16
	v_perm_b32 v243, v223, v222, s17
	v_perm_b32 v227, v242, v240, s18
	v_perm_b32 v231, v242, v240, s19
	v_perm_b32 v235, v243, v241, s18
	v_perm_b32 v239, v243, v241, s19
	s_add_u32 s26, s6, 0x1000
	s_addc_u32 s27, s7, 0
	global_store_dwordx4 v249, v[224:227], s[6:7]
	global_store_dwordx4 v249, v[228:231], s[6:7] offset:2048
	global_store_dwordx4 v249, v[232:235], s[26:27]
	global_store_dwordx4 v249, v[236:239], s[26:27] offset:2048
	s_mov_b64 s[6:7], s[20:21]
	s_waitcnt vmcnt(44)
	v_mul_f32_e32 v64, 0x42800000, v64
	v_mul_f32_e32 v65, 0x42800000, v65
	v_mul_f32_e32 v66, 0x42800000, v66
	v_mul_f32_e32 v67, 0x42800000, v67
	v_med3_f32 v64, v64, s15, v250
	v_med3_f32 v65, v65, s15, v250
	v_med3_f32 v66, v66, s15, v250
	v_med3_f32 v67, v67, s15, v250
	v_cvt_pk_fp8_f32 v192, v64, v65
	v_cvt_pk_fp8_f32 v192, v66, v67 op_sel:[0,0,1]
	v_mul_f32_e32 v68, 0x42800000, v68
	v_mul_f32_e32 v69, 0x42800000, v69
	v_mul_f32_e32 v70, 0x42800000, v70
	v_mul_f32_e32 v71, 0x42800000, v71
	v_med3_f32 v68, v68, s15, v250
	v_med3_f32 v69, v69, s15, v250
	v_med3_f32 v70, v70, s15, v250
	v_med3_f32 v71, v71, s15, v250
	v_cvt_pk_fp8_f32 v193, v68, v69
	v_cvt_pk_fp8_f32 v193, v70, v71 op_sel:[0,0,1]
	v_mul_f32_e32 v72, 0x42800000, v72
	v_mul_f32_e32 v73, 0x42800000, v73
	v_mul_f32_e32 v74, 0x42800000, v74
	v_mul_f32_e32 v75, 0x42800000, v75
	v_med3_f32 v72, v72, s15, v250
	v_med3_f32 v73, v73, s15, v250
	v_med3_f32 v74, v74, s15, v250
	v_med3_f32 v75, v75, s15, v250
	v_cvt_pk_fp8_f32 v194, v72, v73
	v_cvt_pk_fp8_f32 v194, v74, v75 op_sel:[0,0,1]
	v_mul_f32_e32 v76, 0x42800000, v76
	v_mul_f32_e32 v77, 0x42800000, v77
	v_mul_f32_e32 v78, 0x42800000, v78
	v_mul_f32_e32 v79, 0x42800000, v79
	v_med3_f32 v76, v76, s15, v250
	v_med3_f32 v77, v77, s15, v250
	v_med3_f32 v78, v78, s15, v250
	v_med3_f32 v79, v79, s15, v250
	v_cvt_pk_fp8_f32 v195, v76, v77
	v_cvt_pk_fp8_f32 v195, v78, v79 op_sel:[0,0,1]
	v_mul_f32_e32 v80, 0x42800000, v80
	v_mul_f32_e32 v81, 0x42800000, v81
	v_mul_f32_e32 v82, 0x42800000, v82
	v_mul_f32_e32 v83, 0x42800000, v83
	v_med3_f32 v80, v80, s15, v250
	v_med3_f32 v81, v81, s15, v250
	v_med3_f32 v82, v82, s15, v250
	v_med3_f32 v83, v83, s15, v250
	v_cvt_pk_fp8_f32 v196, v80, v81
	v_cvt_pk_fp8_f32 v196, v82, v83 op_sel:[0,0,1]
	v_mul_f32_e32 v84, 0x42800000, v84
	v_mul_f32_e32 v85, 0x42800000, v85
	v_mul_f32_e32 v86, 0x42800000, v86
	v_mul_f32_e32 v87, 0x42800000, v87
	v_med3_f32 v84, v84, s15, v250
	v_med3_f32 v85, v85, s15, v250
	v_med3_f32 v86, v86, s15, v250
	v_med3_f32 v87, v87, s15, v250
	v_cvt_pk_fp8_f32 v197, v84, v85
	v_cvt_pk_fp8_f32 v197, v86, v87 op_sel:[0,0,1]
	v_mul_f32_e32 v88, 0x42800000, v88
	v_mul_f32_e32 v89, 0x42800000, v89
	v_mul_f32_e32 v90, 0x42800000, v90
	v_mul_f32_e32 v91, 0x42800000, v91
	v_med3_f32 v88, v88, s15, v250
	v_med3_f32 v89, v89, s15, v250
	v_med3_f32 v90, v90, s15, v250
	v_med3_f32 v91, v91, s15, v250
	v_cvt_pk_fp8_f32 v198, v88, v89
	v_cvt_pk_fp8_f32 v198, v90, v91 op_sel:[0,0,1]
	v_mul_f32_e32 v92, 0x42800000, v92
	v_mul_f32_e32 v93, 0x42800000, v93
	v_mul_f32_e32 v94, 0x42800000, v94
	v_mul_f32_e32 v95, 0x42800000, v95
	v_med3_f32 v92, v92, s15, v250
	v_med3_f32 v93, v93, s15, v250
	v_med3_f32 v94, v94, s15, v250
	v_med3_f32 v95, v95, s15, v250
	v_cvt_pk_fp8_f32 v199, v92, v93
	v_cvt_pk_fp8_f32 v199, v94, v95 op_sel:[0,0,1]
	v_mul_f32_e32 v96, 0x42800000, v96
	v_mul_f32_e32 v97, 0x42800000, v97
	v_mul_f32_e32 v98, 0x42800000, v98
	v_mul_f32_e32 v99, 0x42800000, v99
	v_med3_f32 v96, v96, s15, v250
	v_med3_f32 v97, v97, s15, v250
	v_med3_f32 v98, v98, s15, v250
	v_med3_f32 v99, v99, s15, v250
	v_cvt_pk_fp8_f32 v200, v96, v97
	v_cvt_pk_fp8_f32 v200, v98, v99 op_sel:[0,0,1]
	v_mul_f32_e32 v100, 0x42800000, v100
	v_mul_f32_e32 v101, 0x42800000, v101
	v_mul_f32_e32 v102, 0x42800000, v102
	v_mul_f32_e32 v103, 0x42800000, v103
	v_med3_f32 v100, v100, s15, v250
	v_med3_f32 v101, v101, s15, v250
	v_med3_f32 v102, v102, s15, v250
	v_med3_f32 v103, v103, s15, v250
	v_cvt_pk_fp8_f32 v201, v100, v101
	v_cvt_pk_fp8_f32 v201, v102, v103 op_sel:[0,0,1]
	v_mul_f32_e32 v104, 0x42800000, v104
	v_mul_f32_e32 v105, 0x42800000, v105
	v_mul_f32_e32 v106, 0x42800000, v106
	v_mul_f32_e32 v107, 0x42800000, v107
	v_med3_f32 v104, v104, s15, v250
	v_med3_f32 v105, v105, s15, v250
	v_med3_f32 v106, v106, s15, v250
	v_med3_f32 v107, v107, s15, v250
	v_cvt_pk_fp8_f32 v202, v104, v105
	v_cvt_pk_fp8_f32 v202, v106, v107 op_sel:[0,0,1]
	v_mul_f32_e32 v108, 0x42800000, v108
	v_mul_f32_e32 v109, 0x42800000, v109
	v_mul_f32_e32 v110, 0x42800000, v110
	v_mul_f32_e32 v111, 0x42800000, v111
	v_med3_f32 v108, v108, s15, v250
	v_med3_f32 v109, v109, s15, v250
	v_med3_f32 v110, v110, s15, v250
	v_med3_f32 v111, v111, s15, v250
	v_cvt_pk_fp8_f32 v203, v108, v109
	v_cvt_pk_fp8_f32 v203, v110, v111 op_sel:[0,0,1]
	v_mul_f32_e32 v112, 0x42800000, v112
	v_mul_f32_e32 v113, 0x42800000, v113
	v_mul_f32_e32 v114, 0x42800000, v114
	v_mul_f32_e32 v115, 0x42800000, v115
	v_med3_f32 v112, v112, s15, v250
	v_med3_f32 v113, v113, s15, v250
	v_med3_f32 v114, v114, s15, v250
	v_med3_f32 v115, v115, s15, v250
	v_cvt_pk_fp8_f32 v204, v112, v113
	v_cvt_pk_fp8_f32 v204, v114, v115 op_sel:[0,0,1]
	v_mul_f32_e32 v116, 0x42800000, v116
	v_mul_f32_e32 v117, 0x42800000, v117
	v_mul_f32_e32 v118, 0x42800000, v118
	v_mul_f32_e32 v119, 0x42800000, v119
	v_med3_f32 v116, v116, s15, v250
	v_med3_f32 v117, v117, s15, v250
	v_med3_f32 v118, v118, s15, v250
	v_med3_f32 v119, v119, s15, v250
	v_cvt_pk_fp8_f32 v205, v116, v117
	v_cvt_pk_fp8_f32 v205, v118, v119 op_sel:[0,0,1]
	v_mul_f32_e32 v120, 0x42800000, v120
	v_mul_f32_e32 v121, 0x42800000, v121
	v_mul_f32_e32 v122, 0x42800000, v122
	v_mul_f32_e32 v123, 0x42800000, v123
	v_med3_f32 v120, v120, s15, v250
	v_med3_f32 v121, v121, s15, v250
	v_med3_f32 v122, v122, s15, v250
	v_med3_f32 v123, v123, s15, v250
	v_cvt_pk_fp8_f32 v206, v120, v121
	v_cvt_pk_fp8_f32 v206, v122, v123 op_sel:[0,0,1]
	v_mul_f32_e32 v124, 0x42800000, v124
	v_mul_f32_e32 v125, 0x42800000, v125
	v_mul_f32_e32 v126, 0x42800000, v126
	v_mul_f32_e32 v127, 0x42800000, v127
	v_med3_f32 v124, v124, s15, v250
	v_med3_f32 v125, v125, s15, v250
	v_med3_f32 v126, v126, s15, v250
	v_med3_f32 v127, v127, s15, v250
	v_cvt_pk_fp8_f32 v207, v124, v125
	v_cvt_pk_fp8_f32 v207, v126, v127 op_sel:[0,0,1]
	s_min_u32 s22, s2, s28
	s_cmp_lt_u32 s22, 0x10000
	s_cbranch_scc0 .Lcv_dn_7
	s_lshr_b32 s23, s22, 11
	s_bfe_u32 s24, s22, 0x40007
	s_and_b32 s25, s22, 0x7f
	s_lshl_b32 s30, s24, 7
	s_lshl_b32 s24, s24, 21
	s_lshl_b32 s22, s25, 7
	s_add_u32 s24, s24, s22
	s_lshl_b32 s25, s25, 16
	s_add_u32 s30, s30, s25
	s_lshl_b32 s22, s23, 25
	s_add_u32 s24, s24, s22
	s_add_u32 s4, s70, s24
	s_addc_u32 s5, s71, 0
	s_lshl_b32 s23, s23, 23
	s_add_u32 s30, s30, s23
	s_add_u32 s30, s30, 0x38ee1c00
	s_add_u32 s20, s92, s30
	s_addc_u32 s21, s93, 0
	s_mov_b32 s14, 0x20000
	s_mov_b64 vcc, -1
	s_branch .Lcv_ld_7

.Lcv_ld_7:
	s_add_u32 s2, s2, s3
	v_cndmask_b32_e32 v246, v245, v244, vcc
	global_load_dwordx4 v[64:67], v246, s[4:5] nt
	s_add_u32 s4, s4, s14
	s_addc_u32 s5, s5, 0
	global_load_dwordx4 v[68:71], v246, s[4:5] nt
	s_add_u32 s4, s4, s14
	s_addc_u32 s5, s5, 0
	global_load_dwordx4 v[72:75], v246, s[4:5] nt
	s_add_u32 s4, s4, s14
	s_addc_u32 s5, s5, 0
	global_load_dwordx4 v[76:79], v246, s[4:5] nt
	s_add_u32 s4, s4, s14
	s_addc_u32 s5, s5, 0
	global_load_dwordx4 v[80:83], v246, s[4:5] nt
	s_add_u32 s4, s4, s14
	s_addc_u32 s5, s5, 0
	global_load_dwordx4 v[84:87], v246, s[4:5] nt
	s_add_u32 s4, s4, s14
	s_addc_u32 s5, s5, 0
	global_load_dwordx4 v[88:91], v246, s[4:5] nt
	s_add_u32 s4, s4, s14
	s_addc_u32 s5, s5, 0
	global_load_dwordx4 v[92:95], v246, s[4:5] nt
	s_add_u32 s4, s4, s14
	s_addc_u32 s5, s5, 0
	global_load_dwordx4 v[96:99], v246, s[4:5] nt
	s_add_u32 s4, s4, s14
	s_addc_u32 s5, s5, 0
	global_load_dwordx4 v[100:103], v246, s[4:5] nt
	s_add_u32 s4, s4, s14
	s_addc_u32 s5, s5, 0
	global_load_dwordx4 v[104:107], v246, s[4:5] nt
	s_add_u32 s4, s4, s14
	s_addc_u32 s5, s5, 0
	global_load_dwordx4 v[108:111], v246, s[4:5] nt
	s_add_u32 s4, s4, s14
	s_addc_u32 s5, s5, 0
	global_load_dwordx4 v[112:115], v246, s[4:5] nt
	s_add_u32 s4, s4, s14
	s_addc_u32 s5, s5, 0
	global_load_dwordx4 v[116:119], v246, s[4:5] nt
	s_add_u32 s4, s4, s14
	s_addc_u32 s5, s5, 0
	global_load_dwordx4 v[120:123], v246, s[4:5] nt
	s_add_u32 s4, s4, s14
	s_addc_u32 s5, s5, 0
	global_load_dwordx4 v[124:127], v246, s[4:5] nt
	ds_write_b32 v247, v192 offset:0
	ds_write_b32 v247, v193 offset:32
	ds_write_b32 v247, v194 offset:64
	ds_write_b32 v247, v195 offset:96
	ds_write_b32 v247, v196 offset:128
	ds_write_b32 v247, v197 offset:160
	ds_write_b32 v247, v198 offset:192
	ds_write_b32 v247, v199 offset:224
	ds_write_b32 v247, v200 offset:256
	ds_write_b32 v247, v201 offset:288
	ds_write_b32 v247, v202 offset:320
	ds_write_b32 v247, v203 offset:352
	ds_write_b32 v247, v204 offset:384
	ds_write_b32 v247, v205 offset:416
	ds_write_b32 v247, v206 offset:448
	ds_write_b32 v247, v207 offset:480
	ds_read_b128 v[208:211], v248 offset:0
	ds_read_b128 v[212:215], v248 offset:16
	ds_read_b128 v[216:219], v248 offset:32
	ds_read_b128 v[220:223], v248 offset:48
	s_waitcnt lgkmcnt(3)
	v_perm_b32 v240, v209, v208, s16
	v_perm_b32 v241, v209, v208, s17
	v_perm_b32 v242, v211, v210, s16
	v_perm_b32 v243, v211, v210, s17
	v_perm_b32 v224, v242, v240, s18
	v_perm_b32 v228, v242, v240, s19
	v_perm_b32 v232, v243, v241, s18
	v_perm_b32 v236, v243, v241, s19
	s_waitcnt lgkmcnt(2)
	v_perm_b32 v240, v213, v212, s16
	v_perm_b32 v241, v213, v212, s17
	v_perm_b32 v242, v215, v214, s16
	v_perm_b32 v243, v215, v214, s17
	v_perm_b32 v225, v242, v240, s18
	v_perm_b32 v229, v242, v240, s19
	v_perm_b32 v233, v243, v241, s18
	v_perm_b32 v237, v243, v241, s19
	s_waitcnt lgkmcnt(1)
	v_perm_b32 v240, v217, v216, s16
	v_perm_b32 v241, v217, v216, s17
	v_perm_b32 v242, v219, v218, s16
	v_perm_b32 v243, v219, v218, s17
	v_perm_b32 v226, v242, v240, s18
	v_perm_b32 v230, v242, v240, s19
	v_perm_b32 v234, v243, v241, s18
	v_perm_b32 v238, v243, v241, s19
	s_waitcnt lgkmcnt(0)
	v_perm_b32 v240, v221, v220, s16
	v_perm_b32 v241, v221, v220, s17
	v_perm_b32 v242, v223, v222, s16
	v_perm_b32 v243, v223, v222, s17
	v_perm_b32 v227, v242, v240, s18
	v_perm_b32 v231, v242, v240, s19
	v_perm_b32 v235, v243, v241, s18
	v_perm_b32 v239, v243, v241, s19
	s_add_u32 s26, s8, 0x1000
	s_addc_u32 s27, s9, 0
	global_store_dwordx4 v249, v[224:227], s[8:9]
	global_store_dwordx4 v249, v[228:231], s[8:9] offset:2048
	global_store_dwordx4 v249, v[232:235], s[26:27]
	global_store_dwordx4 v249, v[236:239], s[26:27] offset:2048
	s_mov_b64 s[8:9], s[20:21]
	s_waitcnt vmcnt(44)
	v_mul_f32_e32 v128, 0x42800000, v128
	v_mul_f32_e32 v129, 0x42800000, v129
	v_mul_f32_e32 v130, 0x42800000, v130
	v_mul_f32_e32 v131, 0x42800000, v131
	v_med3_f32 v128, v128, s15, v250
	v_med3_f32 v129, v129, s15, v250
	v_med3_f32 v130, v130, s15, v250
	v_med3_f32 v131, v131, s15, v250
	v_cvt_pk_fp8_f32 v192, v128, v129
	v_cvt_pk_fp8_f32 v192, v130, v131 op_sel:[0,0,1]
	v_mul_f32_e32 v132, 0x42800000, v132
	v_mul_f32_e32 v133, 0x42800000, v133
	v_mul_f32_e32 v134, 0x42800000, v134
	v_mul_f32_e32 v135, 0x42800000, v135
	v_med3_f32 v132, v132, s15, v250
	v_med3_f32 v133, v133, s15, v250
	v_med3_f32 v134, v134, s15, v250
	v_med3_f32 v135, v135, s15, v250
	v_cvt_pk_fp8_f32 v193, v132, v133
	v_cvt_pk_fp8_f32 v193, v134, v135 op_sel:[0,0,1]
	v_mul_f32_e32 v136, 0x42800000, v136
	v_mul_f32_e32 v137, 0x42800000, v137
	v_mul_f32_e32 v138, 0x42800000, v138
	v_mul_f32_e32 v139, 0x42800000, v139
	v_med3_f32 v136, v136, s15, v250
	v_med3_f32 v137, v137, s15, v250
	v_med3_f32 v138, v138, s15, v250
	v_med3_f32 v139, v139, s15, v250
	v_cvt_pk_fp8_f32 v194, v136, v137
	v_cvt_pk_fp8_f32 v194, v138, v139 op_sel:[0,0,1]
	v_mul_f32_e32 v140, 0x42800000, v140
	v_mul_f32_e32 v141, 0x42800000, v141
	v_mul_f32_e32 v142, 0x42800000, v142
	v_mul_f32_e32 v143, 0x42800000, v143
	v_med3_f32 v140, v140, s15, v250
	v_med3_f32 v141, v141, s15, v250
	v_med3_f32 v142, v142, s15, v250
	v_med3_f32 v143, v143, s15, v250
	v_cvt_pk_fp8_f32 v195, v140, v141
	v_cvt_pk_fp8_f32 v195, v142, v143 op_sel:[0,0,1]
	v_mul_f32_e32 v144, 0x42800000, v144
	v_mul_f32_e32 v145, 0x42800000, v145
	v_mul_f32_e32 v146, 0x42800000, v146
	v_mul_f32_e32 v147, 0x42800000, v147
	v_med3_f32 v144, v144, s15, v250
	v_med3_f32 v145, v145, s15, v250
	v_med3_f32 v146, v146, s15, v250
	v_med3_f32 v147, v147, s15, v250
	v_cvt_pk_fp8_f32 v196, v144, v145
	v_cvt_pk_fp8_f32 v196, v146, v147 op_sel:[0,0,1]
	v_mul_f32_e32 v148, 0x42800000, v148
	v_mul_f32_e32 v149, 0x42800000, v149
	v_mul_f32_e32 v150, 0x42800000, v150
	v_mul_f32_e32 v151, 0x42800000, v151
	v_med3_f32 v148, v148, s15, v250
	v_med3_f32 v149, v149, s15, v250
	v_med3_f32 v150, v150, s15, v250
	v_med3_f32 v151, v151, s15, v250
	v_cvt_pk_fp8_f32 v197, v148, v149
	v_cvt_pk_fp8_f32 v197, v150, v151 op_sel:[0,0,1]
	v_mul_f32_e32 v152, 0x42800000, v152
	v_mul_f32_e32 v153, 0x42800000, v153
	v_mul_f32_e32 v154, 0x42800000, v154
	v_mul_f32_e32 v155, 0x42800000, v155
	v_med3_f32 v152, v152, s15, v250
	v_med3_f32 v153, v153, s15, v250
	v_med3_f32 v154, v154, s15, v250
	v_med3_f32 v155, v155, s15, v250
	v_cvt_pk_fp8_f32 v198, v152, v153
	v_cvt_pk_fp8_f32 v198, v154, v155 op_sel:[0,0,1]
	v_mul_f32_e32 v156, 0x42800000, v156
	v_mul_f32_e32 v157, 0x42800000, v157
	v_mul_f32_e32 v158, 0x42800000, v158
	v_mul_f32_e32 v159, 0x42800000, v159
	v_med3_f32 v156, v156, s15, v250
	v_med3_f32 v157, v157, s15, v250
	v_med3_f32 v158, v158, s15, v250
	v_med3_f32 v159, v159, s15, v250
	v_cvt_pk_fp8_f32 v199, v156, v157
	v_cvt_pk_fp8_f32 v199, v158, v159 op_sel:[0,0,1]
	v_mul_f32_e32 v160, 0x42800000, v160
	v_mul_f32_e32 v161, 0x42800000, v161
	v_mul_f32_e32 v162, 0x42800000, v162
	v_mul_f32_e32 v163, 0x42800000, v163
	v_med3_f32 v160, v160, s15, v250
	v_med3_f32 v161, v161, s15, v250
	v_med3_f32 v162, v162, s15, v250
	v_med3_f32 v163, v163, s15, v250
	v_cvt_pk_fp8_f32 v200, v160, v161
	v_cvt_pk_fp8_f32 v200, v162, v163 op_sel:[0,0,1]
	v_mul_f32_e32 v164, 0x42800000, v164
	v_mul_f32_e32 v165, 0x42800000, v165
	v_mul_f32_e32 v166, 0x42800000, v166
	v_mul_f32_e32 v167, 0x42800000, v167
	v_med3_f32 v164, v164, s15, v250
	v_med3_f32 v165, v165, s15, v250
	v_med3_f32 v166, v166, s15, v250
	v_med3_f32 v167, v167, s15, v250
	v_cvt_pk_fp8_f32 v201, v164, v165
	v_cvt_pk_fp8_f32 v201, v166, v167 op_sel:[0,0,1]
	v_mul_f32_e32 v168, 0x42800000, v168
	v_mul_f32_e32 v169, 0x42800000, v169
	v_mul_f32_e32 v170, 0x42800000, v170
	v_mul_f32_e32 v171, 0x42800000, v171
	v_med3_f32 v168, v168, s15, v250
	v_med3_f32 v169, v169, s15, v250
	v_med3_f32 v170, v170, s15, v250
	v_med3_f32 v171, v171, s15, v250
	v_cvt_pk_fp8_f32 v202, v168, v169
	v_cvt_pk_fp8_f32 v202, v170, v171 op_sel:[0,0,1]
	v_mul_f32_e32 v172, 0x42800000, v172
	v_mul_f32_e32 v173, 0x42800000, v173
	v_mul_f32_e32 v174, 0x42800000, v174
	v_mul_f32_e32 v175, 0x42800000, v175
	v_med3_f32 v172, v172, s15, v250
	v_med3_f32 v173, v173, s15, v250
	v_med3_f32 v174, v174, s15, v250
	v_med3_f32 v175, v175, s15, v250
	v_cvt_pk_fp8_f32 v203, v172, v173
	v_cvt_pk_fp8_f32 v203, v174, v175 op_sel:[0,0,1]
	v_mul_f32_e32 v176, 0x42800000, v176
	v_mul_f32_e32 v177, 0x42800000, v177
	v_mul_f32_e32 v178, 0x42800000, v178
	v_mul_f32_e32 v179, 0x42800000, v179
	v_med3_f32 v176, v176, s15, v250
	v_med3_f32 v177, v177, s15, v250
	v_med3_f32 v178, v178, s15, v250
	v_med3_f32 v179, v179, s15, v250
	v_cvt_pk_fp8_f32 v204, v176, v177
	v_cvt_pk_fp8_f32 v204, v178, v179 op_sel:[0,0,1]
	v_mul_f32_e32 v180, 0x42800000, v180
	v_mul_f32_e32 v181, 0x42800000, v181
	v_mul_f32_e32 v182, 0x42800000, v182
	v_mul_f32_e32 v183, 0x42800000, v183
	v_med3_f32 v180, v180, s15, v250
	v_med3_f32 v181, v181, s15, v250
	v_med3_f32 v182, v182, s15, v250
	v_med3_f32 v183, v183, s15, v250
	v_cvt_pk_fp8_f32 v205, v180, v181
	v_cvt_pk_fp8_f32 v205, v182, v183 op_sel:[0,0,1]
	v_mul_f32_e32 v184, 0x42800000, v184
	v_mul_f32_e32 v185, 0x42800000, v185
	v_mul_f32_e32 v186, 0x42800000, v186
	v_mul_f32_e32 v187, 0x42800000, v187
	v_med3_f32 v184, v184, s15, v250
	v_med3_f32 v185, v185, s15, v250
	v_med3_f32 v186, v186, s15, v250
	v_med3_f32 v187, v187, s15, v250
	v_cvt_pk_fp8_f32 v206, v184, v185
	v_cvt_pk_fp8_f32 v206, v186, v187 op_sel:[0,0,1]
	v_mul_f32_e32 v188, 0x42800000, v188
	v_mul_f32_e32 v189, 0x42800000, v189
	v_mul_f32_e32 v190, 0x42800000, v190
	v_mul_f32_e32 v191, 0x42800000, v191
	v_med3_f32 v188, v188, s15, v250
	v_med3_f32 v189, v189, s15, v250
	v_med3_f32 v190, v190, s15, v250
	v_med3_f32 v191, v191, s15, v250
	v_cvt_pk_fp8_f32 v207, v188, v189
	v_cvt_pk_fp8_f32 v207, v190, v191 op_sel:[0,0,1]
	s_min_u32 s22, s2, s28
	s_cmp_lt_u32 s22, 0x10000
	s_cbranch_scc0 .Lcv_dn_8
	s_lshr_b32 s23, s22, 11
	s_bfe_u32 s24, s22, 0x40007
	s_and_b32 s25, s22, 0x7f
	s_lshl_b32 s30, s24, 7
	s_lshl_b32 s24, s24, 21
	s_lshl_b32 s22, s25, 7
	s_add_u32 s24, s24, s22
	s_lshl_b32 s25, s25, 16
	s_add_u32 s30, s30, s25
	s_lshl_b32 s22, s23, 25
	s_add_u32 s24, s24, s22
	s_add_u32 s4, s70, s24
	s_addc_u32 s5, s71, 0
	s_lshl_b32 s23, s23, 23
	s_add_u32 s30, s30, s23
	s_add_u32 s30, s30, 0x38ee1c00
	s_add_u32 s20, s92, s30
	s_addc_u32 s21, s93, 0
	s_mov_b32 s14, 0x20000
	s_mov_b64 vcc, -1
	s_branch .Lcv_ld_8

.Lcv_ld_8:
	s_add_u32 s2, s2, s3
	v_cndmask_b32_e32 v246, v245, v244, vcc
	global_load_dwordx4 v[128:131], v246, s[4:5] nt
	s_add_u32 s4, s4, s14
	s_addc_u32 s5, s5, 0
	global_load_dwordx4 v[132:135], v246, s[4:5] nt
	s_add_u32 s4, s4, s14
	s_addc_u32 s5, s5, 0
	global_load_dwordx4 v[136:139], v246, s[4:5] nt
	s_add_u32 s4, s4, s14
	s_addc_u32 s5, s5, 0
	global_load_dwordx4 v[140:143], v246, s[4:5] nt
	s_add_u32 s4, s4, s14
	s_addc_u32 s5, s5, 0
	global_load_dwordx4 v[144:147], v246, s[4:5] nt
	s_add_u32 s4, s4, s14
	s_addc_u32 s5, s5, 0
	global_load_dwordx4 v[148:151], v246, s[4:5] nt
	s_add_u32 s4, s4, s14
	s_addc_u32 s5, s5, 0
	global_load_dwordx4 v[152:155], v246, s[4:5] nt
	s_add_u32 s4, s4, s14
	s_addc_u32 s5, s5, 0
	global_load_dwordx4 v[156:159], v246, s[4:5] nt
	s_add_u32 s4, s4, s14
	s_addc_u32 s5, s5, 0
	global_load_dwordx4 v[160:163], v246, s[4:5] nt
	s_add_u32 s4, s4, s14
	s_addc_u32 s5, s5, 0
	global_load_dwordx4 v[164:167], v246, s[4:5] nt
	s_add_u32 s4, s4, s14
	s_addc_u32 s5, s5, 0
	global_load_dwordx4 v[168:171], v246, s[4:5] nt
	s_add_u32 s4, s4, s14
	s_addc_u32 s5, s5, 0
	global_load_dwordx4 v[172:175], v246, s[4:5] nt
	s_add_u32 s4, s4, s14
	s_addc_u32 s5, s5, 0
	global_load_dwordx4 v[176:179], v246, s[4:5] nt
	s_add_u32 s4, s4, s14
	s_addc_u32 s5, s5, 0
	global_load_dwordx4 v[180:183], v246, s[4:5] nt
	s_add_u32 s4, s4, s14
	s_addc_u32 s5, s5, 0
	global_load_dwordx4 v[184:187], v246, s[4:5] nt
	s_add_u32 s4, s4, s14
	s_addc_u32 s5, s5, 0
	global_load_dwordx4 v[188:191], v246, s[4:5] nt
	ds_write_b32 v247, v192 offset:0
	ds_write_b32 v247, v193 offset:32
	ds_write_b32 v247, v194 offset:64
	ds_write_b32 v247, v195 offset:96
	ds_write_b32 v247, v196 offset:128
	ds_write_b32 v247, v197 offset:160
	ds_write_b32 v247, v198 offset:192
	ds_write_b32 v247, v199 offset:224
	ds_write_b32 v247, v200 offset:256
	ds_write_b32 v247, v201 offset:288
	ds_write_b32 v247, v202 offset:320
	ds_write_b32 v247, v203 offset:352
	ds_write_b32 v247, v204 offset:384
	ds_write_b32 v247, v205 offset:416
	ds_write_b32 v247, v206 offset:448
	ds_write_b32 v247, v207 offset:480
	ds_read_b128 v[208:211], v248 offset:0
	ds_read_b128 v[212:215], v248 offset:16
	ds_read_b128 v[216:219], v248 offset:32
	ds_read_b128 v[220:223], v248 offset:48
	s_waitcnt lgkmcnt(3)
	v_perm_b32 v240, v209, v208, s16
	v_perm_b32 v241, v209, v208, s17
	v_perm_b32 v242, v211, v210, s16
	v_perm_b32 v243, v211, v210, s17
	v_perm_b32 v224, v242, v240, s18
	v_perm_b32 v228, v242, v240, s19
	v_perm_b32 v232, v243, v241, s18
	v_perm_b32 v236, v243, v241, s19
	s_waitcnt lgkmcnt(2)
	v_perm_b32 v240, v213, v212, s16
	v_perm_b32 v241, v213, v212, s17
	v_perm_b32 v242, v215, v214, s16
	v_perm_b32 v243, v215, v214, s17
	v_perm_b32 v225, v242, v240, s18
	v_perm_b32 v229, v242, v240, s19
	v_perm_b32 v233, v243, v241, s18
	v_perm_b32 v237, v243, v241, s19
	s_waitcnt lgkmcnt(1)
	v_perm_b32 v240, v217, v216, s16
	v_perm_b32 v241, v217, v216, s17
	v_perm_b32 v242, v219, v218, s16
	v_perm_b32 v243, v219, v218, s17
	v_perm_b32 v226, v242, v240, s18
	v_perm_b32 v230, v242, v240, s19
	v_perm_b32 v234, v243, v241, s18
	v_perm_b32 v238, v243, v241, s19
	s_waitcnt lgkmcnt(0)
	v_perm_b32 v240, v221, v220, s16
	v_perm_b32 v241, v221, v220, s17
	v_perm_b32 v242, v223, v222, s16
	v_perm_b32 v243, v223, v222, s17
	v_perm_b32 v227, v242, v240, s18
	v_perm_b32 v231, v242, v240, s19
	v_perm_b32 v235, v243, v241, s18
	v_perm_b32 v239, v243, v241, s19
	s_add_u32 s26, s10, 0x1000
	s_addc_u32 s27, s11, 0
	global_store_dwordx4 v249, v[224:227], s[10:11]
	global_store_dwordx4 v249, v[228:231], s[10:11] offset:2048
	global_store_dwordx4 v249, v[232:235], s[26:27]
	global_store_dwordx4 v249, v[236:239], s[26:27] offset:2048
	s_mov_b64 s[10:11], s[20:21]
	s_sub_u32 s22, s2, s31
	s_cmp_le_u32 s22, s28
	s_cbranch_scc1 .Lcv_loop
.Lcv_done:
	s_waitcnt vmcnt(0)
.LBB0_311:
	s_mov_b64 s[2:3], 0
